# baseline (speedup 1.0000x reference)
.LBB2_132:
	s_load_dwordx8 s[4:11], s[0:1], 0x0
	s_load_dwordx2 s[12:13], s[0:1], 0x20
	s_load_dwordx2 s[34:35], s[0:1], 0x28
	s_lshr_b32 s24, s2, 0
	s_and_b32 s25, s2, 0
	s_mul_i32 s26, s25, 16
	s_add_u32 s27, s26, 16
	v_lshl_or_b32 v55, s24, 14, v0
	s_waitcnt lgkmcnt(0)
	s_mov_b32 s14, 0x61a80
	s_mov_b32 s15, 0xf4240
	s_mov_b32 s16, 0x155cc0
	v_mov_b32_e32 v34, s4
	v_mov_b32_e32 v37, s5
	v_mov_b32_e32 v35, s6
	v_mov_b32_e32 v38, s7
	v_mov_b32_e32 v36, s8
	v_mov_b32_e32 v39, s9
	v_mov_b32_e32 v43, 0
	v_mov_b32_e32 v47, 0
	v_mov_b32_e32 v49, 0x30d40
	v_mov_b32_e32 v50, 0xfff6d840
	v_mov_b32_e32 v48, 0x61a80
	v_mov_b32_e32 v51, 0x61a80
	v_mov_b32_e32 v52, 0xf4240
	v_mov_b32_e32 v53, 0x30d40
	v_mov_b32_e32 v54, 0x61a80
	v_cmp_gt_u32_e64 s[18:19], s14, v55
	v_cmp_gt_u32_e64 s[20:21], s15, v55
	v_cmp_gt_u32_e64 s[22:23], s16, v55
	s_nop 0
	v_cndmask_b32_e64 v44, v36, v35, s[20:21]
	v_cndmask_b32_e64 v44, v44, v34, s[18:19]
	v_cndmask_b32_e64 v45, v39, v38, s[20:21]
	v_cndmask_b32_e64 v45, v45, v37, s[18:19]
	v_cndmask_b32_e64 v42, v50, v49, s[20:21]
	v_cndmask_b32_e64 v42, v42, v48, s[18:19]
	v_add_u32_e32 v42, v42, v55
	v_cndmask_b32_e64 v42, 0, v42, s[22:23]
	v_lshl_add_u64 v[46:47], v[42:43], 2, v[44:45]
	global_load_dword v3, v[46:47], off
	v_cndmask_b32_e64 v42, v52, v51, s[20:21]
	v_cndmask_b32_e64 v42, v42, 0, s[18:19]
	v_sub_u32_e32 v42, v55, v42
	v_cndmask_b32_e64 v42, 0, v42, s[22:23]
	v_lshl_add_u64 v[46:47], v[42:43], 2, v[44:45]
	global_load_dword v2, v[46:47], off
	v_add_u32_e32 v40, 0x400, v55
	v_cmp_gt_u32_e64 s[18:19], s14, v40
	v_cmp_gt_u32_e64 s[20:21], s15, v40
	v_cmp_gt_u32_e64 s[22:23], s16, v40
	s_nop 0
	v_cndmask_b32_e64 v44, v36, v35, s[20:21]
	v_cndmask_b32_e64 v44, v44, v34, s[18:19]
	v_cndmask_b32_e64 v45, v39, v38, s[20:21]
	v_cndmask_b32_e64 v45, v45, v37, s[18:19]
	v_cndmask_b32_e64 v42, v50, v49, s[20:21]
	v_cndmask_b32_e64 v42, v42, v48, s[18:19]
	v_add_u32_e32 v42, v42, v40
	v_cndmask_b32_e64 v42, 0, v42, s[22:23]
	v_lshl_add_u64 v[46:47], v[42:43], 2, v[44:45]
	global_load_dword v5, v[46:47], off
	v_cndmask_b32_e64 v42, v52, v51, s[20:21]
	v_cndmask_b32_e64 v42, v42, 0, s[18:19]
	v_sub_u32_e32 v42, v40, v42
	v_cndmask_b32_e64 v42, 0, v42, s[22:23]
	v_lshl_add_u64 v[46:47], v[42:43], 2, v[44:45]
	global_load_dword v4, v[46:47], off
	v_add_u32_e32 v40, 0x800, v55
	v_cmp_gt_u32_e64 s[18:19], s14, v40
	v_cmp_gt_u32_e64 s[20:21], s15, v40
	v_cmp_gt_u32_e64 s[22:23], s16, v40
	s_nop 0
	v_cndmask_b32_e64 v44, v36, v35, s[20:21]
	v_cndmask_b32_e64 v44, v44, v34, s[18:19]
	v_cndmask_b32_e64 v45, v39, v38, s[20:21]
	v_cndmask_b32_e64 v45, v45, v37, s[18:19]
	v_cndmask_b32_e64 v42, v50, v49, s[20:21]
	v_cndmask_b32_e64 v42, v42, v48, s[18:19]
	v_add_u32_e32 v42, v42, v40
	v_cndmask_b32_e64 v42, 0, v42, s[22:23]
	v_lshl_add_u64 v[46:47], v[42:43], 2, v[44:45]
	global_load_dword v7, v[46:47], off
	v_cndmask_b32_e64 v42, v52, v51, s[20:21]
	v_cndmask_b32_e64 v42, v42, 0, s[18:19]
	v_sub_u32_e32 v42, v40, v42
	v_cndmask_b32_e64 v42, 0, v42, s[22:23]
	v_lshl_add_u64 v[46:47], v[42:43], 2, v[44:45]
	global_load_dword v6, v[46:47], off
	v_add_u32_e32 v40, 0xc00, v55
	v_cmp_gt_u32_e64 s[18:19], s14, v40
	v_cmp_gt_u32_e64 s[20:21], s15, v40
	v_cmp_gt_u32_e64 s[22:23], s16, v40
	s_nop 0
	v_cndmask_b32_e64 v44, v36, v35, s[20:21]
	v_cndmask_b32_e64 v44, v44, v34, s[18:19]
	v_cndmask_b32_e64 v45, v39, v38, s[20:21]
	v_cndmask_b32_e64 v45, v45, v37, s[18:19]
	v_cndmask_b32_e64 v42, v50, v49, s[20:21]
	v_cndmask_b32_e64 v42, v42, v48, s[18:19]
	v_add_u32_e32 v42, v42, v40
	v_cndmask_b32_e64 v42, 0, v42, s[22:23]
	v_lshl_add_u64 v[46:47], v[42:43], 2, v[44:45]
	global_load_dword v9, v[46:47], off
	v_cndmask_b32_e64 v42, v52, v51, s[20:21]
	v_cndmask_b32_e64 v42, v42, 0, s[18:19]
	v_sub_u32_e32 v42, v40, v42
	v_cndmask_b32_e64 v42, 0, v42, s[22:23]
	v_lshl_add_u64 v[46:47], v[42:43], 2, v[44:45]
	global_load_dword v8, v[46:47], off
	v_add_u32_e32 v40, 0x1000, v55
	v_cmp_gt_u32_e64 s[18:19], s14, v40
	v_cmp_gt_u32_e64 s[20:21], s15, v40
	v_cmp_gt_u32_e64 s[22:23], s16, v40
	s_nop 0
	v_cndmask_b32_e64 v44, v36, v35, s[20:21]
	v_cndmask_b32_e64 v44, v44, v34, s[18:19]
	v_cndmask_b32_e64 v45, v39, v38, s[20:21]
	v_cndmask_b32_e64 v45, v45, v37, s[18:19]
	v_cndmask_b32_e64 v42, v50, v49, s[20:21]
	v_cndmask_b32_e64 v42, v42, v48, s[18:19]
	v_add_u32_e32 v42, v42, v40
	v_cndmask_b32_e64 v42, 0, v42, s[22:23]
	v_lshl_add_u64 v[46:47], v[42:43], 2, v[44:45]
	global_load_dword v11, v[46:47], off
	v_cndmask_b32_e64 v42, v52, v51, s[20:21]
	v_cndmask_b32_e64 v42, v42, 0, s[18:19]
	v_sub_u32_e32 v42, v40, v42
	v_cndmask_b32_e64 v42, 0, v42, s[22:23]
	v_lshl_add_u64 v[46:47], v[42:43], 2, v[44:45]
	global_load_dword v10, v[46:47], off
	v_add_u32_e32 v40, 0x1400, v55
	v_cmp_gt_u32_e64 s[18:19], s14, v40
	v_cmp_gt_u32_e64 s[20:21], s15, v40
	v_cmp_gt_u32_e64 s[22:23], s16, v40
	s_nop 0
	v_cndmask_b32_e64 v44, v36, v35, s[20:21]
	v_cndmask_b32_e64 v44, v44, v34, s[18:19]
	v_cndmask_b32_e64 v45, v39, v38, s[20:21]
	v_cndmask_b32_e64 v45, v45, v37, s[18:19]
	v_cndmask_b32_e64 v42, v50, v49, s[20:21]
	v_cndmask_b32_e64 v42, v42, v48, s[18:19]
	v_add_u32_e32 v42, v42, v40
	v_cndmask_b32_e64 v42, 0, v42, s[22:23]
	v_lshl_add_u64 v[46:47], v[42:43], 2, v[44:45]
	global_load_dword v13, v[46:47], off
	v_cndmask_b32_e64 v42, v52, v51, s[20:21]
	v_cndmask_b32_e64 v42, v42, 0, s[18:19]
	v_sub_u32_e32 v42, v40, v42
	v_cndmask_b32_e64 v42, 0, v42, s[22:23]
	v_lshl_add_u64 v[46:47], v[42:43], 2, v[44:45]
	global_load_dword v12, v[46:47], off
	v_add_u32_e32 v40, 0x1800, v55
	v_cmp_gt_u32_e64 s[18:19], s14, v40
	v_cmp_gt_u32_e64 s[20:21], s15, v40
	v_cmp_gt_u32_e64 s[22:23], s16, v40
	s_nop 0
	v_cndmask_b32_e64 v44, v36, v35, s[20:21]
	v_cndmask_b32_e64 v44, v44, v34, s[18:19]
	v_cndmask_b32_e64 v45, v39, v38, s[20:21]
	v_cndmask_b32_e64 v45, v45, v37, s[18:19]
	v_cndmask_b32_e64 v42, v50, v49, s[20:21]
	v_cndmask_b32_e64 v42, v42, v48, s[18:19]
	v_add_u32_e32 v42, v42, v40
	v_cndmask_b32_e64 v42, 0, v42, s[22:23]
	v_lshl_add_u64 v[46:47], v[42:43], 2, v[44:45]
	global_load_dword v15, v[46:47], off
	v_cndmask_b32_e64 v42, v52, v51, s[20:21]
	v_cndmask_b32_e64 v42, v42, 0, s[18:19]
	v_sub_u32_e32 v42, v40, v42
	v_cndmask_b32_e64 v42, 0, v42, s[22:23]
	v_lshl_add_u64 v[46:47], v[42:43], 2, v[44:45]
	global_load_dword v14, v[46:47], off
	v_add_u32_e32 v40, 0x1c00, v55
	v_cmp_gt_u32_e64 s[18:19], s14, v40
	v_cmp_gt_u32_e64 s[20:21], s15, v40
	v_cmp_gt_u32_e64 s[22:23], s16, v40
	s_nop 0
	v_cndmask_b32_e64 v44, v36, v35, s[20:21]
	v_cndmask_b32_e64 v44, v44, v34, s[18:19]
	v_cndmask_b32_e64 v45, v39, v38, s[20:21]
	v_cndmask_b32_e64 v45, v45, v37, s[18:19]
	v_cndmask_b32_e64 v42, v50, v49, s[20:21]
	v_cndmask_b32_e64 v42, v42, v48, s[18:19]
	v_add_u32_e32 v42, v42, v40
	v_cndmask_b32_e64 v42, 0, v42, s[22:23]
	v_lshl_add_u64 v[46:47], v[42:43], 2, v[44:45]
	global_load_dword v17, v[46:47], off
	v_cndmask_b32_e64 v42, v52, v51, s[20:21]
	v_cndmask_b32_e64 v42, v42, 0, s[18:19]
	v_sub_u32_e32 v42, v40, v42
	v_cndmask_b32_e64 v42, 0, v42, s[22:23]
	v_lshl_add_u64 v[46:47], v[42:43], 2, v[44:45]
	global_load_dword v16, v[46:47], off
	v_add_u32_e32 v40, 0x2000, v55
	v_cmp_gt_u32_e64 s[18:19], s14, v40
	v_cmp_gt_u32_e64 s[20:21], s15, v40
	v_cmp_gt_u32_e64 s[22:23], s16, v40
	s_nop 0
	v_cndmask_b32_e64 v44, v36, v35, s[20:21]
	v_cndmask_b32_e64 v44, v44, v34, s[18:19]
	v_cndmask_b32_e64 v45, v39, v38, s[20:21]
	v_cndmask_b32_e64 v45, v45, v37, s[18:19]
	v_cndmask_b32_e64 v42, v50, v49, s[20:21]
	v_cndmask_b32_e64 v42, v42, v48, s[18:19]
	v_add_u32_e32 v42, v42, v40
	v_cndmask_b32_e64 v42, 0, v42, s[22:23]
	v_lshl_add_u64 v[46:47], v[42:43], 2, v[44:45]
	global_load_dword v19, v[46:47], off
	v_cndmask_b32_e64 v42, v52, v51, s[20:21]
	v_cndmask_b32_e64 v42, v42, 0, s[18:19]
	v_sub_u32_e32 v42, v40, v42
	v_cndmask_b32_e64 v42, 0, v42, s[22:23]
	v_lshl_add_u64 v[46:47], v[42:43], 2, v[44:45]
	global_load_dword v18, v[46:47], off
	v_add_u32_e32 v40, 0x2400, v55
	v_cmp_gt_u32_e64 s[18:19], s14, v40
	v_cmp_gt_u32_e64 s[20:21], s15, v40
	v_cmp_gt_u32_e64 s[22:23], s16, v40
	s_nop 0
	v_cndmask_b32_e64 v44, v36, v35, s[20:21]
	v_cndmask_b32_e64 v44, v44, v34, s[18:19]
	v_cndmask_b32_e64 v45, v39, v38, s[20:21]
	v_cndmask_b32_e64 v45, v45, v37, s[18:19]
	v_cndmask_b32_e64 v42, v50, v49, s[20:21]
	v_cndmask_b32_e64 v42, v42, v48, s[18:19]
	v_add_u32_e32 v42, v42, v40
	v_cndmask_b32_e64 v42, 0, v42, s[22:23]
	v_lshl_add_u64 v[46:47], v[42:43], 2, v[44:45]
	global_load_dword v21, v[46:47], off
	v_cndmask_b32_e64 v42, v52, v51, s[20:21]
	v_cndmask_b32_e64 v42, v42, 0, s[18:19]
	v_sub_u32_e32 v42, v40, v42
	v_cndmask_b32_e64 v42, 0, v42, s[22:23]
	v_lshl_add_u64 v[46:47], v[42:43], 2, v[44:45]
	global_load_dword v20, v[46:47], off
	v_add_u32_e32 v40, 0x2800, v55
	v_cmp_gt_u32_e64 s[18:19], s14, v40
	v_cmp_gt_u32_e64 s[20:21], s15, v40
	v_cmp_gt_u32_e64 s[22:23], s16, v40
	s_nop 0
	v_cndmask_b32_e64 v44, v36, v35, s[20:21]
	v_cndmask_b32_e64 v44, v44, v34, s[18:19]
	v_cndmask_b32_e64 v45, v39, v38, s[20:21]
	v_cndmask_b32_e64 v45, v45, v37, s[18:19]
	v_cndmask_b32_e64 v42, v50, v49, s[20:21]
	v_cndmask_b32_e64 v42, v42, v48, s[18:19]
	v_add_u32_e32 v42, v42, v40
	v_cndmask_b32_e64 v42, 0, v42, s[22:23]
	v_lshl_add_u64 v[46:47], v[42:43], 2, v[44:45]
	global_load_dword v23, v[46:47], off
	v_cndmask_b32_e64 v42, v52, v51, s[20:21]
	v_cndmask_b32_e64 v42, v42, 0, s[18:19]
	v_sub_u32_e32 v42, v40, v42
	v_cndmask_b32_e64 v42, 0, v42, s[22:23]
	v_lshl_add_u64 v[46:47], v[42:43], 2, v[44:45]
	global_load_dword v22, v[46:47], off
	v_add_u32_e32 v40, 0x2c00, v55
	v_cmp_gt_u32_e64 s[18:19], s14, v40
	v_cmp_gt_u32_e64 s[20:21], s15, v40
	v_cmp_gt_u32_e64 s[22:23], s16, v40
	s_nop 0
	v_cndmask_b32_e64 v44, v36, v35, s[20:21]
	v_cndmask_b32_e64 v44, v44, v34, s[18:19]
	v_cndmask_b32_e64 v45, v39, v38, s[20:21]
	v_cndmask_b32_e64 v45, v45, v37, s[18:19]
	v_cndmask_b32_e64 v42, v50, v49, s[20:21]
	v_cndmask_b32_e64 v42, v42, v48, s[18:19]
	v_add_u32_e32 v42, v42, v40
	v_cndmask_b32_e64 v42, 0, v42, s[22:23]
	v_lshl_add_u64 v[46:47], v[42:43], 2, v[44:45]
	global_load_dword v25, v[46:47], off
	v_cndmask_b32_e64 v42, v52, v51, s[20:21]
	v_cndmask_b32_e64 v42, v42, 0, s[18:19]
	v_sub_u32_e32 v42, v40, v42
	v_cndmask_b32_e64 v42, 0, v42, s[22:23]
	v_lshl_add_u64 v[46:47], v[42:43], 2, v[44:45]
	global_load_dword v24, v[46:47], off
	v_add_u32_e32 v40, 0x3000, v55
	v_cmp_gt_u32_e64 s[18:19], s14, v40
	v_cmp_gt_u32_e64 s[20:21], s15, v40
	v_cmp_gt_u32_e64 s[22:23], s16, v40
	s_nop 0
	v_cndmask_b32_e64 v44, v36, v35, s[20:21]
	v_cndmask_b32_e64 v44, v44, v34, s[18:19]
	v_cndmask_b32_e64 v45, v39, v38, s[20:21]
	v_cndmask_b32_e64 v45, v45, v37, s[18:19]
	v_cndmask_b32_e64 v42, v50, v49, s[20:21]
	v_cndmask_b32_e64 v42, v42, v48, s[18:19]
	v_add_u32_e32 v42, v42, v40
	v_cndmask_b32_e64 v42, 0, v42, s[22:23]
	v_lshl_add_u64 v[46:47], v[42:43], 2, v[44:45]
	global_load_dword v27, v[46:47], off
	v_cndmask_b32_e64 v42, v52, v51, s[20:21]
	v_cndmask_b32_e64 v42, v42, 0, s[18:19]
	v_sub_u32_e32 v42, v40, v42
	v_cndmask_b32_e64 v42, 0, v42, s[22:23]
	v_lshl_add_u64 v[46:47], v[42:43], 2, v[44:45]
	global_load_dword v26, v[46:47], off
	v_add_u32_e32 v40, 0x3400, v55
	v_cmp_gt_u32_e64 s[18:19], s14, v40
	v_cmp_gt_u32_e64 s[20:21], s15, v40
	v_cmp_gt_u32_e64 s[22:23], s16, v40
	s_nop 0
	v_cndmask_b32_e64 v44, v36, v35, s[20:21]
	v_cndmask_b32_e64 v44, v44, v34, s[18:19]
	v_cndmask_b32_e64 v45, v39, v38, s[20:21]
	v_cndmask_b32_e64 v45, v45, v37, s[18:19]
	v_cndmask_b32_e64 v42, v50, v49, s[20:21]
	v_cndmask_b32_e64 v42, v42, v48, s[18:19]
	v_add_u32_e32 v42, v42, v40
	v_cndmask_b32_e64 v42, 0, v42, s[22:23]
	v_lshl_add_u64 v[46:47], v[42:43], 2, v[44:45]
	global_load_dword v29, v[46:47], off
	v_cndmask_b32_e64 v42, v52, v51, s[20:21]
	v_cndmask_b32_e64 v42, v42, 0, s[18:19]
	v_sub_u32_e32 v42, v40, v42
	v_cndmask_b32_e64 v42, 0, v42, s[22:23]
	v_lshl_add_u64 v[46:47], v[42:43], 2, v[44:45]
	global_load_dword v28, v[46:47], off
	v_add_u32_e32 v40, 0x3800, v55
	v_cmp_gt_u32_e64 s[18:19], s14, v40
	v_cmp_gt_u32_e64 s[20:21], s15, v40
	v_cmp_gt_u32_e64 s[22:23], s16, v40
	s_nop 0
	v_cndmask_b32_e64 v44, v36, v35, s[20:21]
	v_cndmask_b32_e64 v44, v44, v34, s[18:19]
	v_cndmask_b32_e64 v45, v39, v38, s[20:21]
	v_cndmask_b32_e64 v45, v45, v37, s[18:19]
	v_cndmask_b32_e64 v42, v50, v49, s[20:21]
	v_cndmask_b32_e64 v42, v42, v48, s[18:19]
	v_add_u32_e32 v42, v42, v40
	v_cndmask_b32_e64 v42, 0, v42, s[22:23]
	v_lshl_add_u64 v[46:47], v[42:43], 2, v[44:45]
	global_load_dword v31, v[46:47], off
	v_cndmask_b32_e64 v42, v52, v51, s[20:21]
	v_cndmask_b32_e64 v42, v42, 0, s[18:19]
	v_sub_u32_e32 v42, v40, v42
	v_cndmask_b32_e64 v42, 0, v42, s[22:23]
	v_lshl_add_u64 v[46:47], v[42:43], 2, v[44:45]
	global_load_dword v30, v[46:47], off
	v_add_u32_e32 v40, 0x3c00, v55
	v_cmp_gt_u32_e64 s[18:19], s14, v40
	v_cmp_gt_u32_e64 s[20:21], s15, v40
	v_cmp_gt_u32_e64 s[22:23], s16, v40
	s_nop 0
	v_cndmask_b32_e64 v44, v36, v35, s[20:21]
	v_cndmask_b32_e64 v44, v44, v34, s[18:19]
	v_cndmask_b32_e64 v45, v39, v38, s[20:21]
	v_cndmask_b32_e64 v45, v45, v37, s[18:19]
	v_cndmask_b32_e64 v42, v50, v49, s[20:21]
	v_cndmask_b32_e64 v42, v42, v48, s[18:19]
	v_add_u32_e32 v42, v42, v40
	v_cndmask_b32_e64 v42, 0, v42, s[22:23]
	v_lshl_add_u64 v[46:47], v[42:43], 2, v[44:45]
	global_load_dword v33, v[46:47], off
	v_cndmask_b32_e64 v42, v52, v51, s[20:21]
	v_cndmask_b32_e64 v42, v42, 0, s[18:19]
	v_sub_u32_e32 v42, v40, v42
	v_cndmask_b32_e64 v42, 0, v42, s[22:23]
	v_lshl_add_u64 v[46:47], v[42:43], 2, v[44:45]
	global_load_dword v32, v[46:47], off
	v_mov_b32_e32 v34, 0
	v_mov_b32_e32 v35, 0
	v_mov_b32_e32 v36, 0
	v_mov_b32_e32 v37, 0
	v_lshlrev_b32_e32 v38, 3, v0
	v_cmp_gt_u32_e32 vcc, 0x224, v0
	s_and_saveexec_b64 s[36:37], vcc
	s_cbranch_execz .Lsc_nohist
	global_load_dwordx2 v[40:41], v38, s[10:11]
	v_add_u32_e32 v39, 0x1120, v38
	global_load_dwordx2 v[42:43], v39, s[10:11]
	v_add_u32_e32 v39, 0x2240, v38
	global_load_dwordx2 v[44:45], v39, s[10:11]
	v_add_u32_e32 v39, 0x3360, v38
	global_load_dwordx2 v[46:47], v39, s[10:11]
	v_add_u32_e32 v39, 0x4480, v38
	global_load_dwordx2 v[48:49], v39, s[10:11]
	v_add_u32_e32 v39, 0x55a0, v38
	global_load_dwordx2 v[50:51], v39, s[10:11]
	v_add_u32_e32 v39, 0x66c0, v38
	global_load_dwordx2 v[52:53], v39, s[10:11]
	v_add_u32_e32 v39, 0x77e0, v38
	global_load_dwordx2 v[54:55], v39, s[10:11]
	v_add_u32_e32 v39, 0x8900, v38
	global_load_dwordx2 v[56:57], v39, s[10:11]
	v_add_u32_e32 v39, 0x9a20, v38
	global_load_dwordx2 v[58:59], v39, s[10:11]
	v_add_u32_e32 v39, 0xab40, v38
	global_load_dwordx2 v[60:61], v39, s[10:11]
	v_add_u32_e32 v39, 0xbc60, v38
	global_load_dwordx2 v[62:63], v39, s[10:11]
	s_waitcnt vmcnt(11)
	s_cmp_gt_u32 s24, 0
	s_cselect_b32 s3, 1, 0
	v_add_u32_e32 v34, v34, v40
	v_add_u32_e32 v35, v35, v41
	v_mad_u32_u24 v36, v40, s3, v36
	v_mad_u32_u24 v37, v41, s3, v37
	v_add_u32_e32 v39, 0xcd80, v38
	global_load_dwordx2 v[40:41], v39, s[10:11]
	s_waitcnt vmcnt(11)
	s_cmp_gt_u32 s24, 1
	s_cselect_b32 s3, 1, 0
	v_add_u32_e32 v34, v34, v42
	v_add_u32_e32 v35, v35, v43
	v_mad_u32_u24 v36, v42, s3, v36
	v_mad_u32_u24 v37, v43, s3, v37
	v_add_u32_e32 v39, 0xdea0, v38
	global_load_dwordx2 v[42:43], v39, s[10:11]
	s_waitcnt vmcnt(11)
	s_cmp_gt_u32 s24, 2
	s_cselect_b32 s3, 1, 0
	v_add_u32_e32 v34, v34, v44
	v_add_u32_e32 v35, v35, v45
	v_mad_u32_u24 v36, v44, s3, v36
	v_mad_u32_u24 v37, v45, s3, v37
	v_add_u32_e32 v39, 0xefc0, v38
	global_load_dwordx2 v[44:45], v39, s[10:11]
	s_waitcnt vmcnt(11)
	s_cmp_gt_u32 s24, 3
	s_cselect_b32 s3, 1, 0
	v_add_u32_e32 v34, v34, v46
	v_add_u32_e32 v35, v35, v47
	v_mad_u32_u24 v36, v46, s3, v36
	v_mad_u32_u24 v37, v47, s3, v37
	v_add_u32_e32 v39, 0x100e0, v38
	global_load_dwordx2 v[46:47], v39, s[10:11]
	s_waitcnt vmcnt(11)
	s_cmp_gt_u32 s24, 4
	s_cselect_b32 s3, 1, 0
	v_add_u32_e32 v34, v34, v48
	v_add_u32_e32 v35, v35, v49
	v_mad_u32_u24 v36, v48, s3, v36
	v_mad_u32_u24 v37, v49, s3, v37
	v_add_u32_e32 v39, 0x11200, v38
	global_load_dwordx2 v[48:49], v39, s[10:11]
	s_waitcnt vmcnt(11)
	s_cmp_gt_u32 s24, 5
	s_cselect_b32 s3, 1, 0
	v_add_u32_e32 v34, v34, v50
	v_add_u32_e32 v35, v35, v51
	v_mad_u32_u24 v36, v50, s3, v36
	v_mad_u32_u24 v37, v51, s3, v37
	v_add_u32_e32 v39, 0x12320, v38
	global_load_dwordx2 v[50:51], v39, s[10:11]
	s_waitcnt vmcnt(11)
	s_cmp_gt_u32 s24, 6
	s_cselect_b32 s3, 1, 0
	v_add_u32_e32 v34, v34, v52
	v_add_u32_e32 v35, v35, v53
	v_mad_u32_u24 v36, v52, s3, v36
	v_mad_u32_u24 v37, v53, s3, v37
	v_add_u32_e32 v39, 0x13440, v38
	global_load_dwordx2 v[52:53], v39, s[10:11]
	s_waitcnt vmcnt(11)
	s_cmp_gt_u32 s24, 7
	s_cselect_b32 s3, 1, 0
	v_add_u32_e32 v34, v34, v54
	v_add_u32_e32 v35, v35, v55
	v_mad_u32_u24 v36, v54, s3, v36
	v_mad_u32_u24 v37, v55, s3, v37
	v_add_u32_e32 v39, 0x14560, v38
	global_load_dwordx2 v[54:55], v39, s[10:11]
	s_waitcnt vmcnt(11)
	s_cmp_gt_u32 s24, 8
	s_cselect_b32 s3, 1, 0
	v_add_u32_e32 v34, v34, v56
	v_add_u32_e32 v35, v35, v57
	v_mad_u32_u24 v36, v56, s3, v36
	v_mad_u32_u24 v37, v57, s3, v37
	v_add_u32_e32 v39, 0x15680, v38
	global_load_dwordx2 v[56:57], v39, s[10:11]
	s_waitcnt vmcnt(11)
	s_cmp_gt_u32 s24, 9
	s_cselect_b32 s3, 1, 0
	v_add_u32_e32 v34, v34, v58
	v_add_u32_e32 v35, v35, v59
	v_mad_u32_u24 v36, v58, s3, v36
	v_mad_u32_u24 v37, v59, s3, v37
	v_add_u32_e32 v39, 0x167a0, v38
	global_load_dwordx2 v[58:59], v39, s[10:11]
	s_waitcnt vmcnt(11)
	s_cmp_gt_u32 s24, 10
	s_cselect_b32 s3, 1, 0
	v_add_u32_e32 v34, v34, v60
	v_add_u32_e32 v35, v35, v61
	v_mad_u32_u24 v36, v60, s3, v36
	v_mad_u32_u24 v37, v61, s3, v37
	v_add_u32_e32 v39, 0x178c0, v38
	global_load_dwordx2 v[60:61], v39, s[10:11]
	s_waitcnt vmcnt(11)
	s_cmp_gt_u32 s24, 11
	s_cselect_b32 s3, 1, 0
	v_add_u32_e32 v34, v34, v62
	v_add_u32_e32 v35, v35, v63
	v_mad_u32_u24 v36, v62, s3, v36
	v_mad_u32_u24 v37, v63, s3, v37
	v_add_u32_e32 v39, 0x189e0, v38
	global_load_dwordx2 v[62:63], v39, s[10:11]
	s_waitcnt vmcnt(11)
	s_cmp_gt_u32 s24, 12
	s_cselect_b32 s3, 1, 0
	v_add_u32_e32 v34, v34, v40
	v_add_u32_e32 v35, v35, v41
	v_mad_u32_u24 v36, v40, s3, v36
	v_mad_u32_u24 v37, v41, s3, v37
	v_add_u32_e32 v39, 0x19b00, v38
	global_load_dwordx2 v[40:41], v39, s[10:11]
	s_waitcnt vmcnt(11)
	s_cmp_gt_u32 s24, 13
	s_cselect_b32 s3, 1, 0
	v_add_u32_e32 v34, v34, v42
	v_add_u32_e32 v35, v35, v43
	v_mad_u32_u24 v36, v42, s3, v36
	v_mad_u32_u24 v37, v43, s3, v37
	v_add_u32_e32 v39, 0x1ac20, v38
	global_load_dwordx2 v[42:43], v39, s[10:11]
	s_waitcnt vmcnt(11)
	s_cmp_gt_u32 s24, 14
	s_cselect_b32 s3, 1, 0
	v_add_u32_e32 v34, v34, v44
	v_add_u32_e32 v35, v35, v45
	v_mad_u32_u24 v36, v44, s3, v36
	v_mad_u32_u24 v37, v45, s3, v37
	v_add_u32_e32 v39, 0x1bd40, v38
	global_load_dwordx2 v[44:45], v39, s[10:11]
	s_waitcnt vmcnt(11)
	s_cmp_gt_u32 s24, 15
	s_cselect_b32 s3, 1, 0
	v_add_u32_e32 v34, v34, v46
	v_add_u32_e32 v35, v35, v47
	v_mad_u32_u24 v36, v46, s3, v36
	v_mad_u32_u24 v37, v47, s3, v37
	v_add_u32_e32 v39, 0x1ce60, v38
	global_load_dwordx2 v[46:47], v39, s[10:11]
	s_waitcnt vmcnt(11)
	s_cmp_gt_u32 s24, 16
	s_cselect_b32 s3, 1, 0
	v_add_u32_e32 v34, v34, v48
	v_add_u32_e32 v35, v35, v49
	v_mad_u32_u24 v36, v48, s3, v36
	v_mad_u32_u24 v37, v49, s3, v37
	v_add_u32_e32 v39, 0x1df80, v38
	global_load_dwordx2 v[48:49], v39, s[10:11]
	s_waitcnt vmcnt(11)
	s_cmp_gt_u32 s24, 17
	s_cselect_b32 s3, 1, 0
	v_add_u32_e32 v34, v34, v50
	v_add_u32_e32 v35, v35, v51
	v_mad_u32_u24 v36, v50, s3, v36
	v_mad_u32_u24 v37, v51, s3, v37
	v_add_u32_e32 v39, 0x1f0a0, v38
	global_load_dwordx2 v[50:51], v39, s[10:11]
	s_waitcnt vmcnt(11)
	s_cmp_gt_u32 s24, 18
	s_cselect_b32 s3, 1, 0
	v_add_u32_e32 v34, v34, v52
	v_add_u32_e32 v35, v35, v53
	v_mad_u32_u24 v36, v52, s3, v36
	v_mad_u32_u24 v37, v53, s3, v37
	v_add_u32_e32 v39, 0x201c0, v38
	global_load_dwordx2 v[52:53], v39, s[10:11]
	s_waitcnt vmcnt(11)
	s_cmp_gt_u32 s24, 19
	s_cselect_b32 s3, 1, 0
	v_add_u32_e32 v34, v34, v54
	v_add_u32_e32 v35, v35, v55
	v_mad_u32_u24 v36, v54, s3, v36
	v_mad_u32_u24 v37, v55, s3, v37
	v_add_u32_e32 v39, 0x212e0, v38
	global_load_dwordx2 v[54:55], v39, s[10:11]
	s_waitcnt vmcnt(11)
	s_cmp_gt_u32 s24, 20
	s_cselect_b32 s3, 1, 0
	v_add_u32_e32 v34, v34, v56
	v_add_u32_e32 v35, v35, v57
	v_mad_u32_u24 v36, v56, s3, v36
	v_mad_u32_u24 v37, v57, s3, v37
	v_add_u32_e32 v39, 0x22400, v38
	global_load_dwordx2 v[56:57], v39, s[10:11]
	s_waitcnt vmcnt(11)
	s_cmp_gt_u32 s24, 21
	s_cselect_b32 s3, 1, 0
	v_add_u32_e32 v34, v34, v58
	v_add_u32_e32 v35, v35, v59
	v_mad_u32_u24 v36, v58, s3, v36
	v_mad_u32_u24 v37, v59, s3, v37
	v_add_u32_e32 v39, 0x23520, v38
	global_load_dwordx2 v[58:59], v39, s[10:11]
	s_waitcnt vmcnt(11)
	s_cmp_gt_u32 s24, 22
	s_cselect_b32 s3, 1, 0
	v_add_u32_e32 v34, v34, v60
	v_add_u32_e32 v35, v35, v61
	v_mad_u32_u24 v36, v60, s3, v36
	v_mad_u32_u24 v37, v61, s3, v37
	v_add_u32_e32 v39, 0x24640, v38
	global_load_dwordx2 v[60:61], v39, s[10:11]
	s_waitcnt vmcnt(11)
	s_cmp_gt_u32 s24, 23
	s_cselect_b32 s3, 1, 0
	v_add_u32_e32 v34, v34, v62
	v_add_u32_e32 v35, v35, v63
	v_mad_u32_u24 v36, v62, s3, v36
	v_mad_u32_u24 v37, v63, s3, v37
	v_add_u32_e32 v39, 0x25760, v38
	global_load_dwordx2 v[62:63], v39, s[10:11]
	s_waitcnt vmcnt(11)
	s_cmp_gt_u32 s24, 24
	s_cselect_b32 s3, 1, 0
	v_add_u32_e32 v34, v34, v40
	v_add_u32_e32 v35, v35, v41
	v_mad_u32_u24 v36, v40, s3, v36
	v_mad_u32_u24 v37, v41, s3, v37
	v_add_u32_e32 v39, 0x26880, v38
	global_load_dwordx2 v[40:41], v39, s[10:11]
	s_waitcnt vmcnt(11)
	s_cmp_gt_u32 s24, 25
	s_cselect_b32 s3, 1, 0
	v_add_u32_e32 v34, v34, v42
	v_add_u32_e32 v35, v35, v43
	v_mad_u32_u24 v36, v42, s3, v36
	v_mad_u32_u24 v37, v43, s3, v37
	v_add_u32_e32 v39, 0x279a0, v38
	global_load_dwordx2 v[42:43], v39, s[10:11]
	s_waitcnt vmcnt(11)
	s_cmp_gt_u32 s24, 26
	s_cselect_b32 s3, 1, 0
	v_add_u32_e32 v34, v34, v44
	v_add_u32_e32 v35, v35, v45
	v_mad_u32_u24 v36, v44, s3, v36
	v_mad_u32_u24 v37, v45, s3, v37
	v_add_u32_e32 v39, 0x28ac0, v38
	global_load_dwordx2 v[44:45], v39, s[10:11]
	s_waitcnt vmcnt(11)
	s_cmp_gt_u32 s24, 27
	s_cselect_b32 s3, 1, 0
	v_add_u32_e32 v34, v34, v46
	v_add_u32_e32 v35, v35, v47
	v_mad_u32_u24 v36, v46, s3, v36
	v_mad_u32_u24 v37, v47, s3, v37
	v_add_u32_e32 v39, 0x29be0, v38
	global_load_dwordx2 v[46:47], v39, s[10:11]
	s_waitcnt vmcnt(11)
	s_cmp_gt_u32 s24, 28
	s_cselect_b32 s3, 1, 0
	v_add_u32_e32 v34, v34, v48
	v_add_u32_e32 v35, v35, v49
	v_mad_u32_u24 v36, v48, s3, v36
	v_mad_u32_u24 v37, v49, s3, v37
	v_add_u32_e32 v39, 0x2ad00, v38
	global_load_dwordx2 v[48:49], v39, s[10:11]
	s_waitcnt vmcnt(11)
	s_cmp_gt_u32 s24, 29
	s_cselect_b32 s3, 1, 0
	v_add_u32_e32 v34, v34, v50
	v_add_u32_e32 v35, v35, v51
	v_mad_u32_u24 v36, v50, s3, v36
	v_mad_u32_u24 v37, v51, s3, v37
	v_add_u32_e32 v39, 0x2be20, v38
	global_load_dwordx2 v[50:51], v39, s[10:11]
	s_waitcnt vmcnt(11)
	s_cmp_gt_u32 s24, 30
	s_cselect_b32 s3, 1, 0
	v_add_u32_e32 v34, v34, v52
	v_add_u32_e32 v35, v35, v53
	v_mad_u32_u24 v36, v52, s3, v36
	v_mad_u32_u24 v37, v53, s3, v37
	v_add_u32_e32 v39, 0x2cf40, v38
	global_load_dwordx2 v[52:53], v39, s[10:11]
	s_waitcnt vmcnt(11)
	s_cmp_gt_u32 s24, 31
	s_cselect_b32 s3, 1, 0
	v_add_u32_e32 v34, v34, v54
	v_add_u32_e32 v35, v35, v55
	v_mad_u32_u24 v36, v54, s3, v36
	v_mad_u32_u24 v37, v55, s3, v37
	v_add_u32_e32 v39, 0x2e060, v38
	global_load_dwordx2 v[54:55], v39, s[10:11]
	s_waitcnt vmcnt(11)
	s_cmp_gt_u32 s24, 32
	s_cselect_b32 s3, 1, 0
	v_add_u32_e32 v34, v34, v56
	v_add_u32_e32 v35, v35, v57
	v_mad_u32_u24 v36, v56, s3, v36
	v_mad_u32_u24 v37, v57, s3, v37
	v_add_u32_e32 v39, 0x2f180, v38
	global_load_dwordx2 v[56:57], v39, s[10:11]
	s_waitcnt vmcnt(11)
	s_cmp_gt_u32 s24, 33
	s_cselect_b32 s3, 1, 0
	v_add_u32_e32 v34, v34, v58
	v_add_u32_e32 v35, v35, v59
	v_mad_u32_u24 v36, v58, s3, v36
	v_mad_u32_u24 v37, v59, s3, v37
	v_add_u32_e32 v39, 0x302a0, v38
	global_load_dwordx2 v[58:59], v39, s[10:11]
	s_waitcnt vmcnt(11)
	s_cmp_gt_u32 s24, 34
	s_cselect_b32 s3, 1, 0
	v_add_u32_e32 v34, v34, v60
	v_add_u32_e32 v35, v35, v61
	v_mad_u32_u24 v36, v60, s3, v36
	v_mad_u32_u24 v37, v61, s3, v37
	v_add_u32_e32 v39, 0x313c0, v38
	global_load_dwordx2 v[60:61], v39, s[10:11]
	s_waitcnt vmcnt(11)
	s_cmp_gt_u32 s24, 35
	s_cselect_b32 s3, 1, 0
	v_add_u32_e32 v34, v34, v62
	v_add_u32_e32 v35, v35, v63
	v_mad_u32_u24 v36, v62, s3, v36
	v_mad_u32_u24 v37, v63, s3, v37
	v_add_u32_e32 v39, 0x324e0, v38
	global_load_dwordx2 v[62:63], v39, s[10:11]
	s_waitcnt vmcnt(11)
	s_cmp_gt_u32 s24, 36
	s_cselect_b32 s3, 1, 0
	v_add_u32_e32 v34, v34, v40
	v_add_u32_e32 v35, v35, v41
	v_mad_u32_u24 v36, v40, s3, v36
	v_mad_u32_u24 v37, v41, s3, v37
	v_add_u32_e32 v39, 0x33600, v38
	global_load_dwordx2 v[40:41], v39, s[10:11]
	s_waitcnt vmcnt(11)
	s_cmp_gt_u32 s24, 37
	s_cselect_b32 s3, 1, 0
	v_add_u32_e32 v34, v34, v42
	v_add_u32_e32 v35, v35, v43
	v_mad_u32_u24 v36, v42, s3, v36
	v_mad_u32_u24 v37, v43, s3, v37
	v_add_u32_e32 v39, 0x34720, v38
	global_load_dwordx2 v[42:43], v39, s[10:11]
	s_waitcnt vmcnt(11)
	s_cmp_gt_u32 s24, 38
	s_cselect_b32 s3, 1, 0
	v_add_u32_e32 v34, v34, v44
	v_add_u32_e32 v35, v35, v45
	v_mad_u32_u24 v36, v44, s3, v36
	v_mad_u32_u24 v37, v45, s3, v37
	v_add_u32_e32 v39, 0x35840, v38
	global_load_dwordx2 v[44:45], v39, s[10:11]
	s_waitcnt vmcnt(11)
	s_cmp_gt_u32 s24, 39
	s_cselect_b32 s3, 1, 0
	v_add_u32_e32 v34, v34, v46
	v_add_u32_e32 v35, v35, v47
	v_mad_u32_u24 v36, v46, s3, v36
	v_mad_u32_u24 v37, v47, s3, v37
	v_add_u32_e32 v39, 0x36960, v38
	global_load_dwordx2 v[46:47], v39, s[10:11]
	s_waitcnt vmcnt(11)
	s_cmp_gt_u32 s24, 40
	s_cselect_b32 s3, 1, 0
	v_add_u32_e32 v34, v34, v48
	v_add_u32_e32 v35, v35, v49
	v_mad_u32_u24 v36, v48, s3, v36
	v_mad_u32_u24 v37, v49, s3, v37
	v_add_u32_e32 v39, 0x37a80, v38
	global_load_dwordx2 v[48:49], v39, s[10:11]
	s_waitcnt vmcnt(11)
	s_cmp_gt_u32 s24, 41
	s_cselect_b32 s3, 1, 0
	v_add_u32_e32 v34, v34, v50
	v_add_u32_e32 v35, v35, v51
	v_mad_u32_u24 v36, v50, s3, v36
	v_mad_u32_u24 v37, v51, s3, v37
	v_add_u32_e32 v39, 0x38ba0, v38
	global_load_dwordx2 v[50:51], v39, s[10:11]
	s_waitcnt vmcnt(11)
	s_cmp_gt_u32 s24, 42
	s_cselect_b32 s3, 1, 0
	v_add_u32_e32 v34, v34, v52
	v_add_u32_e32 v35, v35, v53
	v_mad_u32_u24 v36, v52, s3, v36
	v_mad_u32_u24 v37, v53, s3, v37
	v_add_u32_e32 v39, 0x39cc0, v38
	global_load_dwordx2 v[52:53], v39, s[10:11]
	s_waitcnt vmcnt(11)
	s_cmp_gt_u32 s24, 43
	s_cselect_b32 s3, 1, 0
	v_add_u32_e32 v34, v34, v54
	v_add_u32_e32 v35, v35, v55
	v_mad_u32_u24 v36, v54, s3, v36
	v_mad_u32_u24 v37, v55, s3, v37
	v_add_u32_e32 v39, 0x3ade0, v38
	global_load_dwordx2 v[54:55], v39, s[10:11]
	s_waitcnt vmcnt(11)
	s_cmp_gt_u32 s24, 44
	s_cselect_b32 s3, 1, 0
	v_add_u32_e32 v34, v34, v56
	v_add_u32_e32 v35, v35, v57
	v_mad_u32_u24 v36, v56, s3, v36
	v_mad_u32_u24 v37, v57, s3, v37
	v_add_u32_e32 v39, 0x3bf00, v38
	global_load_dwordx2 v[56:57], v39, s[10:11]
	s_waitcnt vmcnt(11)
	s_cmp_gt_u32 s24, 45
	s_cselect_b32 s3, 1, 0
	v_add_u32_e32 v34, v34, v58
	v_add_u32_e32 v35, v35, v59
	v_mad_u32_u24 v36, v58, s3, v36
	v_mad_u32_u24 v37, v59, s3, v37
	v_add_u32_e32 v39, 0x3d020, v38
	global_load_dwordx2 v[58:59], v39, s[10:11]
	s_waitcnt vmcnt(11)
	s_cmp_gt_u32 s24, 46
	s_cselect_b32 s3, 1, 0
	v_add_u32_e32 v34, v34, v60
	v_add_u32_e32 v35, v35, v61
	v_mad_u32_u24 v36, v60, s3, v36
	v_mad_u32_u24 v37, v61, s3, v37
	v_add_u32_e32 v39, 0x3e140, v38
	global_load_dwordx2 v[60:61], v39, s[10:11]
	s_waitcnt vmcnt(11)
	s_cmp_gt_u32 s24, 47
	s_cselect_b32 s3, 1, 0
	v_add_u32_e32 v34, v34, v62
	v_add_u32_e32 v35, v35, v63
	v_mad_u32_u24 v36, v62, s3, v36
	v_mad_u32_u24 v37, v63, s3, v37
	v_add_u32_e32 v39, 0x3f260, v38
	global_load_dwordx2 v[62:63], v39, s[10:11]
	s_waitcnt vmcnt(11)
	s_cmp_gt_u32 s24, 48
	s_cselect_b32 s3, 1, 0
	v_add_u32_e32 v34, v34, v40
	v_add_u32_e32 v35, v35, v41
	v_mad_u32_u24 v36, v40, s3, v36
	v_mad_u32_u24 v37, v41, s3, v37
	v_add_u32_e32 v39, 0x40380, v38
	global_load_dwordx2 v[40:41], v39, s[10:11]
	s_waitcnt vmcnt(11)
	s_cmp_gt_u32 s24, 49
	s_cselect_b32 s3, 1, 0
	v_add_u32_e32 v34, v34, v42
	v_add_u32_e32 v35, v35, v43
	v_mad_u32_u24 v36, v42, s3, v36
	v_mad_u32_u24 v37, v43, s3, v37
	v_add_u32_e32 v39, 0x414a0, v38
	global_load_dwordx2 v[42:43], v39, s[10:11]
	s_waitcnt vmcnt(11)
	s_cmp_gt_u32 s24, 50
	s_cselect_b32 s3, 1, 0
	v_add_u32_e32 v34, v34, v44
	v_add_u32_e32 v35, v35, v45
	v_mad_u32_u24 v36, v44, s3, v36
	v_mad_u32_u24 v37, v45, s3, v37
	v_add_u32_e32 v39, 0x425c0, v38
	global_load_dwordx2 v[44:45], v39, s[10:11]
	s_waitcnt vmcnt(11)
	s_cmp_gt_u32 s24, 51
	s_cselect_b32 s3, 1, 0
	v_add_u32_e32 v34, v34, v46
	v_add_u32_e32 v35, v35, v47
	v_mad_u32_u24 v36, v46, s3, v36
	v_mad_u32_u24 v37, v47, s3, v37
	v_add_u32_e32 v39, 0x436e0, v38
	global_load_dwordx2 v[46:47], v39, s[10:11]
	s_waitcnt vmcnt(11)
	s_cmp_gt_u32 s24, 52
	s_cselect_b32 s3, 1, 0
	v_add_u32_e32 v34, v34, v48
	v_add_u32_e32 v35, v35, v49
	v_mad_u32_u24 v36, v48, s3, v36
	v_mad_u32_u24 v37, v49, s3, v37
	v_add_u32_e32 v39, 0x44800, v38
	global_load_dwordx2 v[48:49], v39, s[10:11]
	s_waitcnt vmcnt(11)
	s_cmp_gt_u32 s24, 53
	s_cselect_b32 s3, 1, 0
	v_add_u32_e32 v34, v34, v50
	v_add_u32_e32 v35, v35, v51
	v_mad_u32_u24 v36, v50, s3, v36
	v_mad_u32_u24 v37, v51, s3, v37
	v_add_u32_e32 v39, 0x45920, v38
	global_load_dwordx2 v[50:51], v39, s[10:11]
	s_waitcnt vmcnt(11)
	s_cmp_gt_u32 s24, 54
	s_cselect_b32 s3, 1, 0
	v_add_u32_e32 v34, v34, v52
	v_add_u32_e32 v35, v35, v53
	v_mad_u32_u24 v36, v52, s3, v36
	v_mad_u32_u24 v37, v53, s3, v37
	v_add_u32_e32 v39, 0x46a40, v38
	global_load_dwordx2 v[52:53], v39, s[10:11]
	s_waitcnt vmcnt(11)
	s_cmp_gt_u32 s24, 55
	s_cselect_b32 s3, 1, 0
	v_add_u32_e32 v34, v34, v54
	v_add_u32_e32 v35, v35, v55
	v_mad_u32_u24 v36, v54, s3, v36
	v_mad_u32_u24 v37, v55, s3, v37
	v_add_u32_e32 v39, 0x47b60, v38
	global_load_dwordx2 v[54:55], v39, s[10:11]
	s_waitcnt vmcnt(11)
	s_cmp_gt_u32 s24, 56
	s_cselect_b32 s3, 1, 0
	v_add_u32_e32 v34, v34, v56
	v_add_u32_e32 v35, v35, v57
	v_mad_u32_u24 v36, v56, s3, v36
	v_mad_u32_u24 v37, v57, s3, v37
	v_add_u32_e32 v39, 0x48c80, v38
	global_load_dwordx2 v[56:57], v39, s[10:11]
	s_waitcnt vmcnt(11)
	s_cmp_gt_u32 s24, 57
	s_cselect_b32 s3, 1, 0
	v_add_u32_e32 v34, v34, v58
	v_add_u32_e32 v35, v35, v59
	v_mad_u32_u24 v36, v58, s3, v36
	v_mad_u32_u24 v37, v59, s3, v37
	v_add_u32_e32 v39, 0x49da0, v38
	global_load_dwordx2 v[58:59], v39, s[10:11]
	s_waitcnt vmcnt(11)
	s_cmp_gt_u32 s24, 58
	s_cselect_b32 s3, 1, 0
	v_add_u32_e32 v34, v34, v60
	v_add_u32_e32 v35, v35, v61
	v_mad_u32_u24 v36, v60, s3, v36
	v_mad_u32_u24 v37, v61, s3, v37
	v_add_u32_e32 v39, 0x4aec0, v38
	global_load_dwordx2 v[60:61], v39, s[10:11]
	s_waitcnt vmcnt(11)
	s_cmp_gt_u32 s24, 59
	s_cselect_b32 s3, 1, 0
	v_add_u32_e32 v34, v34, v62
	v_add_u32_e32 v35, v35, v63
	v_mad_u32_u24 v36, v62, s3, v36
	v_mad_u32_u24 v37, v63, s3, v37
	v_add_u32_e32 v39, 0x4bfe0, v38
	global_load_dwordx2 v[62:63], v39, s[10:11]
	s_waitcnt vmcnt(11)
	s_cmp_gt_u32 s24, 60
	s_cselect_b32 s3, 1, 0
	v_add_u32_e32 v34, v34, v40
	v_add_u32_e32 v35, v35, v41
	v_mad_u32_u24 v36, v40, s3, v36
	v_mad_u32_u24 v37, v41, s3, v37
	v_add_u32_e32 v39, 0x4d100, v38
	global_load_dwordx2 v[40:41], v39, s[10:11]
	s_waitcnt vmcnt(11)
	s_cmp_gt_u32 s24, 61
	s_cselect_b32 s3, 1, 0
	v_add_u32_e32 v34, v34, v42
	v_add_u32_e32 v35, v35, v43
	v_mad_u32_u24 v36, v42, s3, v36
	v_mad_u32_u24 v37, v43, s3, v37
	v_add_u32_e32 v39, 0x4e220, v38
	global_load_dwordx2 v[42:43], v39, s[10:11]
	s_waitcnt vmcnt(11)
	s_cmp_gt_u32 s24, 62
	s_cselect_b32 s3, 1, 0
	v_add_u32_e32 v34, v34, v44
	v_add_u32_e32 v35, v35, v45
	v_mad_u32_u24 v36, v44, s3, v36
	v_mad_u32_u24 v37, v45, s3, v37
	v_add_u32_e32 v39, 0x4f340, v38
	global_load_dwordx2 v[44:45], v39, s[10:11]
	s_waitcnt vmcnt(11)
	s_cmp_gt_u32 s24, 63
	s_cselect_b32 s3, 1, 0
	v_add_u32_e32 v34, v34, v46
	v_add_u32_e32 v35, v35, v47
	v_mad_u32_u24 v36, v46, s3, v36
	v_mad_u32_u24 v37, v47, s3, v37
	v_add_u32_e32 v39, 0x50460, v38
	global_load_dwordx2 v[46:47], v39, s[10:11]
	s_waitcnt vmcnt(11)
	s_cmp_gt_u32 s24, 64
	s_cselect_b32 s3, 1, 0
	v_add_u32_e32 v34, v34, v48
	v_add_u32_e32 v35, v35, v49
	v_mad_u32_u24 v36, v48, s3, v36
	v_mad_u32_u24 v37, v49, s3, v37
	v_add_u32_e32 v39, 0x51580, v38
	global_load_dwordx2 v[48:49], v39, s[10:11]
	s_waitcnt vmcnt(11)
	s_cmp_gt_u32 s24, 65
	s_cselect_b32 s3, 1, 0
	v_add_u32_e32 v34, v34, v50
	v_add_u32_e32 v35, v35, v51
	v_mad_u32_u24 v36, v50, s3, v36
	v_mad_u32_u24 v37, v51, s3, v37
	v_add_u32_e32 v39, 0x526a0, v38
	global_load_dwordx2 v[50:51], v39, s[10:11]
	s_waitcnt vmcnt(11)
	s_cmp_gt_u32 s24, 66
	s_cselect_b32 s3, 1, 0
	v_add_u32_e32 v34, v34, v52
	v_add_u32_e32 v35, v35, v53
	v_mad_u32_u24 v36, v52, s3, v36
	v_mad_u32_u24 v37, v53, s3, v37
	v_add_u32_e32 v39, 0x537c0, v38
	global_load_dwordx2 v[52:53], v39, s[10:11]
	s_waitcnt vmcnt(11)
	s_cmp_gt_u32 s24, 67
	s_cselect_b32 s3, 1, 0
	v_add_u32_e32 v34, v34, v54
	v_add_u32_e32 v35, v35, v55
	v_mad_u32_u24 v36, v54, s3, v36
	v_mad_u32_u24 v37, v55, s3, v37
	v_add_u32_e32 v39, 0x548e0, v38
	global_load_dwordx2 v[54:55], v39, s[10:11]
	s_waitcnt vmcnt(11)
	s_cmp_gt_u32 s24, 68
	s_cselect_b32 s3, 1, 0
	v_add_u32_e32 v34, v34, v56
	v_add_u32_e32 v35, v35, v57
	v_mad_u32_u24 v36, v56, s3, v36
	v_mad_u32_u24 v37, v57, s3, v37
	v_add_u32_e32 v39, 0x55a00, v38
	global_load_dwordx2 v[56:57], v39, s[10:11]
	s_waitcnt vmcnt(11)
	s_cmp_gt_u32 s24, 69
	s_cselect_b32 s3, 1, 0
	v_add_u32_e32 v34, v34, v58
	v_add_u32_e32 v35, v35, v59
	v_mad_u32_u24 v36, v58, s3, v36
	v_mad_u32_u24 v37, v59, s3, v37
	v_add_u32_e32 v39, 0x56b20, v38
	global_load_dwordx2 v[58:59], v39, s[10:11]
	s_waitcnt vmcnt(11)
	s_cmp_gt_u32 s24, 70
	s_cselect_b32 s3, 1, 0
	v_add_u32_e32 v34, v34, v60
	v_add_u32_e32 v35, v35, v61
	v_mad_u32_u24 v36, v60, s3, v36
	v_mad_u32_u24 v37, v61, s3, v37
	v_add_u32_e32 v39, 0x57c40, v38
	global_load_dwordx2 v[60:61], v39, s[10:11]
	s_waitcnt vmcnt(11)
	s_cmp_gt_u32 s24, 71
	s_cselect_b32 s3, 1, 0
	v_add_u32_e32 v34, v34, v62
	v_add_u32_e32 v35, v35, v63
	v_mad_u32_u24 v36, v62, s3, v36
	v_mad_u32_u24 v37, v63, s3, v37
	v_add_u32_e32 v39, 0x58d60, v38
	global_load_dwordx2 v[62:63], v39, s[10:11]
	s_waitcnt vmcnt(11)
	s_cmp_gt_u32 s24, 72
	s_cselect_b32 s3, 1, 0
	v_add_u32_e32 v34, v34, v40
	v_add_u32_e32 v35, v35, v41
	v_mad_u32_u24 v36, v40, s3, v36
	v_mad_u32_u24 v37, v41, s3, v37
	v_add_u32_e32 v39, 0x59e80, v38
	global_load_dwordx2 v[40:41], v39, s[10:11]
	s_waitcnt vmcnt(11)
	s_cmp_gt_u32 s24, 73
	s_cselect_b32 s3, 1, 0
	v_add_u32_e32 v34, v34, v42
	v_add_u32_e32 v35, v35, v43
	v_mad_u32_u24 v36, v42, s3, v36
	v_mad_u32_u24 v37, v43, s3, v37
	v_add_u32_e32 v39, 0x5afa0, v38
	global_load_dwordx2 v[42:43], v39, s[10:11]
	s_waitcnt vmcnt(11)
	s_cmp_gt_u32 s24, 74
	s_cselect_b32 s3, 1, 0
	v_add_u32_e32 v34, v34, v44
	v_add_u32_e32 v35, v35, v45
	v_mad_u32_u24 v36, v44, s3, v36
	v_mad_u32_u24 v37, v45, s3, v37
	s_waitcnt vmcnt(10)
	s_cmp_gt_u32 s24, 75
	s_cselect_b32 s3, 1, 0
	v_add_u32_e32 v34, v34, v46
	v_add_u32_e32 v35, v35, v47
	v_mad_u32_u24 v36, v46, s3, v36
	v_mad_u32_u24 v37, v47, s3, v37
	s_waitcnt vmcnt(9)
	s_cmp_gt_u32 s24, 76
	s_cselect_b32 s3, 1, 0
	v_add_u32_e32 v34, v34, v48
	v_add_u32_e32 v35, v35, v49
	v_mad_u32_u24 v36, v48, s3, v36
	v_mad_u32_u24 v37, v49, s3, v37
	s_waitcnt vmcnt(8)
	s_cmp_gt_u32 s24, 77
	s_cselect_b32 s3, 1, 0
	v_add_u32_e32 v34, v34, v50
	v_add_u32_e32 v35, v35, v51
	v_mad_u32_u24 v36, v50, s3, v36
	v_mad_u32_u24 v37, v51, s3, v37
	s_waitcnt vmcnt(7)
	s_cmp_gt_u32 s24, 78
	s_cselect_b32 s3, 1, 0
	v_add_u32_e32 v34, v34, v52
	v_add_u32_e32 v35, v35, v53
	v_mad_u32_u24 v36, v52, s3, v36
	v_mad_u32_u24 v37, v53, s3, v37
	s_waitcnt vmcnt(6)
	s_cmp_gt_u32 s24, 79
	s_cselect_b32 s3, 1, 0
	v_add_u32_e32 v34, v34, v54
	v_add_u32_e32 v35, v35, v55
	v_mad_u32_u24 v36, v54, s3, v36
	v_mad_u32_u24 v37, v55, s3, v37
	s_waitcnt vmcnt(5)
	s_cmp_gt_u32 s24, 80
	s_cselect_b32 s3, 1, 0
	v_add_u32_e32 v34, v34, v56
	v_add_u32_e32 v35, v35, v57
	v_mad_u32_u24 v36, v56, s3, v36
	v_mad_u32_u24 v37, v57, s3, v37
	s_waitcnt vmcnt(4)
	s_cmp_gt_u32 s24, 81
	s_cselect_b32 s3, 1, 0
	v_add_u32_e32 v34, v34, v58
	v_add_u32_e32 v35, v35, v59
	v_mad_u32_u24 v36, v58, s3, v36
	v_mad_u32_u24 v37, v59, s3, v37
	s_waitcnt vmcnt(3)
	s_cmp_gt_u32 s24, 82
	s_cselect_b32 s3, 1, 0
	v_add_u32_e32 v34, v34, v60
	v_add_u32_e32 v35, v35, v61
	v_mad_u32_u24 v36, v60, s3, v36
	v_mad_u32_u24 v37, v61, s3, v37
	s_waitcnt vmcnt(2)
	s_cmp_gt_u32 s24, 83
	s_cselect_b32 s3, 1, 0
	v_add_u32_e32 v34, v34, v62
	v_add_u32_e32 v35, v35, v63
	v_mad_u32_u24 v36, v62, s3, v36
	v_mad_u32_u24 v37, v63, s3, v37
	s_waitcnt vmcnt(1)
	s_cmp_gt_u32 s24, 84
	s_cselect_b32 s3, 1, 0
	v_add_u32_e32 v34, v34, v40
	v_add_u32_e32 v35, v35, v41
	v_mad_u32_u24 v36, v40, s3, v36
	v_mad_u32_u24 v37, v41, s3, v37
	s_waitcnt vmcnt(0)
	s_cmp_gt_u32 s24, 85
	s_cselect_b32 s3, 1, 0
	v_add_u32_e32 v34, v34, v42
	v_add_u32_e32 v35, v35, v43
	v_mad_u32_u24 v36, v42, s3, v36
	v_mad_u32_u24 v37, v43, s3, v37
.Lsc_nohist:
	s_mov_b64 exec, s[36:37]
	s_waitcnt vmcnt(0)
	v_mov_b32_e32 v53, 0x30d40
	v_mov_b32_e32 v54, 0x61a80
	v_lshl_or_b32 v55, s24, 14, v0
	v_mov_b32_e32 v44, -1
	v_cmp_gt_u32_e64 s[18:19], s14, v55
	v_cmp_gt_u32_e64 s[20:21], s15, v55
	v_cmp_gt_u32_e64 s[22:23], s16, v55
	s_nop 0
	v_cndmask_b32_e64 v42, v54, v53, s[20:21]
	v_cndmask_b32_e64 v42, v42, 0, s[18:19]
	v_add_u32_e32 v3, v3, v42
	v_cndmask_b32_e64 v3, v44, v3, s[22:23]
	v_cndmask_b32_e64 v2, 0, v2, s[22:23]
	v_add_u32_e32 v40, 0x400, v55
	v_cmp_gt_u32_e64 s[18:19], s14, v40
	v_cmp_gt_u32_e64 s[20:21], s15, v40
	v_cmp_gt_u32_e64 s[22:23], s16, v40
	s_nop 0
	v_cndmask_b32_e64 v42, v54, v53, s[20:21]
	v_cndmask_b32_e64 v42, v42, 0, s[18:19]
	v_add_u32_e32 v5, v5, v42
	v_cndmask_b32_e64 v5, v44, v5, s[22:23]
	v_cndmask_b32_e64 v4, 0, v4, s[22:23]
	v_add_u32_e32 v40, 0x800, v55
	v_cmp_gt_u32_e64 s[18:19], s14, v40
	v_cmp_gt_u32_e64 s[20:21], s15, v40
	v_cmp_gt_u32_e64 s[22:23], s16, v40
	s_nop 0
	v_cndmask_b32_e64 v42, v54, v53, s[20:21]
	v_cndmask_b32_e64 v42, v42, 0, s[18:19]
	v_add_u32_e32 v7, v7, v42
	v_cndmask_b32_e64 v7, v44, v7, s[22:23]
	v_cndmask_b32_e64 v6, 0, v6, s[22:23]
	v_add_u32_e32 v40, 0xc00, v55
	v_cmp_gt_u32_e64 s[18:19], s14, v40
	v_cmp_gt_u32_e64 s[20:21], s15, v40
	v_cmp_gt_u32_e64 s[22:23], s16, v40
	s_nop 0
	v_cndmask_b32_e64 v42, v54, v53, s[20:21]
	v_cndmask_b32_e64 v42, v42, 0, s[18:19]
	v_add_u32_e32 v9, v9, v42
	v_cndmask_b32_e64 v9, v44, v9, s[22:23]
	v_cndmask_b32_e64 v8, 0, v8, s[22:23]
	v_add_u32_e32 v40, 0x1000, v55
	v_cmp_gt_u32_e64 s[18:19], s14, v40
	v_cmp_gt_u32_e64 s[20:21], s15, v40
	v_cmp_gt_u32_e64 s[22:23], s16, v40
	s_nop 0
	v_cndmask_b32_e64 v42, v54, v53, s[20:21]
	v_cndmask_b32_e64 v42, v42, 0, s[18:19]
	v_add_u32_e32 v11, v11, v42
	v_cndmask_b32_e64 v11, v44, v11, s[22:23]
	v_cndmask_b32_e64 v10, 0, v10, s[22:23]
	v_add_u32_e32 v40, 0x1400, v55
	v_cmp_gt_u32_e64 s[18:19], s14, v40
	v_cmp_gt_u32_e64 s[20:21], s15, v40
	v_cmp_gt_u32_e64 s[22:23], s16, v40
	s_nop 0
	v_cndmask_b32_e64 v42, v54, v53, s[20:21]
	v_cndmask_b32_e64 v42, v42, 0, s[18:19]
	v_add_u32_e32 v13, v13, v42
	v_cndmask_b32_e64 v13, v44, v13, s[22:23]
	v_cndmask_b32_e64 v12, 0, v12, s[22:23]
	v_add_u32_e32 v40, 0x1800, v55
	v_cmp_gt_u32_e64 s[18:19], s14, v40
	v_cmp_gt_u32_e64 s[20:21], s15, v40
	v_cmp_gt_u32_e64 s[22:23], s16, v40
	s_nop 0
	v_cndmask_b32_e64 v42, v54, v53, s[20:21]
	v_cndmask_b32_e64 v42, v42, 0, s[18:19]
	v_add_u32_e32 v15, v15, v42
	v_cndmask_b32_e64 v15, v44, v15, s[22:23]
	v_cndmask_b32_e64 v14, 0, v14, s[22:23]
	v_add_u32_e32 v40, 0x1c00, v55
	v_cmp_gt_u32_e64 s[18:19], s14, v40
	v_cmp_gt_u32_e64 s[20:21], s15, v40
	v_cmp_gt_u32_e64 s[22:23], s16, v40
	s_nop 0
	v_cndmask_b32_e64 v42, v54, v53, s[20:21]
	v_cndmask_b32_e64 v42, v42, 0, s[18:19]
	v_add_u32_e32 v17, v17, v42
	v_cndmask_b32_e64 v17, v44, v17, s[22:23]
	v_cndmask_b32_e64 v16, 0, v16, s[22:23]
	v_add_u32_e32 v40, 0x2000, v55
	v_cmp_gt_u32_e64 s[18:19], s14, v40
	v_cmp_gt_u32_e64 s[20:21], s15, v40
	v_cmp_gt_u32_e64 s[22:23], s16, v40
	s_nop 0
	v_cndmask_b32_e64 v42, v54, v53, s[20:21]
	v_cndmask_b32_e64 v42, v42, 0, s[18:19]
	v_add_u32_e32 v19, v19, v42
	v_cndmask_b32_e64 v19, v44, v19, s[22:23]
	v_cndmask_b32_e64 v18, 0, v18, s[22:23]
	v_add_u32_e32 v40, 0x2400, v55
	v_cmp_gt_u32_e64 s[18:19], s14, v40
	v_cmp_gt_u32_e64 s[20:21], s15, v40
	v_cmp_gt_u32_e64 s[22:23], s16, v40
	s_nop 0
	v_cndmask_b32_e64 v42, v54, v53, s[20:21]
	v_cndmask_b32_e64 v42, v42, 0, s[18:19]
	v_add_u32_e32 v21, v21, v42
	v_cndmask_b32_e64 v21, v44, v21, s[22:23]
	v_cndmask_b32_e64 v20, 0, v20, s[22:23]
	v_add_u32_e32 v40, 0x2800, v55
	v_cmp_gt_u32_e64 s[18:19], s14, v40
	v_cmp_gt_u32_e64 s[20:21], s15, v40
	v_cmp_gt_u32_e64 s[22:23], s16, v40
	s_nop 0
	v_cndmask_b32_e64 v42, v54, v53, s[20:21]
	v_cndmask_b32_e64 v42, v42, 0, s[18:19]
	v_add_u32_e32 v23, v23, v42
	v_cndmask_b32_e64 v23, v44, v23, s[22:23]
	v_cndmask_b32_e64 v22, 0, v22, s[22:23]
	v_add_u32_e32 v40, 0x2c00, v55
	v_cmp_gt_u32_e64 s[18:19], s14, v40
	v_cmp_gt_u32_e64 s[20:21], s15, v40
	v_cmp_gt_u32_e64 s[22:23], s16, v40
	s_nop 0
	v_cndmask_b32_e64 v42, v54, v53, s[20:21]
	v_cndmask_b32_e64 v42, v42, 0, s[18:19]
	v_add_u32_e32 v25, v25, v42
	v_cndmask_b32_e64 v25, v44, v25, s[22:23]
	v_cndmask_b32_e64 v24, 0, v24, s[22:23]
	v_add_u32_e32 v40, 0x3000, v55
	v_cmp_gt_u32_e64 s[18:19], s14, v40
	v_cmp_gt_u32_e64 s[20:21], s15, v40
	v_cmp_gt_u32_e64 s[22:23], s16, v40
	s_nop 0
	v_cndmask_b32_e64 v42, v54, v53, s[20:21]
	v_cndmask_b32_e64 v42, v42, 0, s[18:19]
	v_add_u32_e32 v27, v27, v42
	v_cndmask_b32_e64 v27, v44, v27, s[22:23]
	v_cndmask_b32_e64 v26, 0, v26, s[22:23]
	v_add_u32_e32 v40, 0x3400, v55
	v_cmp_gt_u32_e64 s[18:19], s14, v40
	v_cmp_gt_u32_e64 s[20:21], s15, v40
	v_cmp_gt_u32_e64 s[22:23], s16, v40
	s_nop 0
	v_cndmask_b32_e64 v42, v54, v53, s[20:21]
	v_cndmask_b32_e64 v42, v42, 0, s[18:19]
	v_add_u32_e32 v29, v29, v42
	v_cndmask_b32_e64 v29, v44, v29, s[22:23]
	v_cndmask_b32_e64 v28, 0, v28, s[22:23]
	v_add_u32_e32 v40, 0x3800, v55
	v_cmp_gt_u32_e64 s[18:19], s14, v40
	v_cmp_gt_u32_e64 s[20:21], s15, v40
	v_cmp_gt_u32_e64 s[22:23], s16, v40
	s_nop 0
	v_cndmask_b32_e64 v42, v54, v53, s[20:21]
	v_cndmask_b32_e64 v42, v42, 0, s[18:19]
	v_add_u32_e32 v31, v31, v42
	v_cndmask_b32_e64 v31, v44, v31, s[22:23]
	v_cndmask_b32_e64 v30, 0, v30, s[22:23]
	v_add_u32_e32 v40, 0x3c00, v55
	v_cmp_gt_u32_e64 s[18:19], s14, v40
	v_cmp_gt_u32_e64 s[20:21], s15, v40
	v_cmp_gt_u32_e64 s[22:23], s16, v40
	s_nop 0
	v_cndmask_b32_e64 v42, v54, v53, s[20:21]
	v_cndmask_b32_e64 v42, v42, 0, s[18:19]
	v_add_u32_e32 v33, v33, v42
	v_cndmask_b32_e64 v33, v44, v33, s[22:23]
	v_cndmask_b32_e64 v32, 0, v32, s[22:23]
	v_add_u32_e32 v38, v34, v35
	v_mov_b32_e32 v39, v38
	s_nop 1
	v_add_u32_dpp v39, v39, v39 row_shr:1 row_mask:0xf bank_mask:0xf bound_ctrl:0
	s_nop 1
	v_add_u32_dpp v39, v39, v39 row_shr:2 row_mask:0xf bank_mask:0xf bound_ctrl:0
	s_nop 1
	v_add_u32_dpp v39, v39, v39 row_shr:4 row_mask:0xf bank_mask:0xf bound_ctrl:0
	s_nop 1
	v_add_u32_dpp v39, v39, v39 row_shr:8 row_mask:0xf bank_mask:0xf bound_ctrl:0
	s_nop 1
	v_add_u32_dpp v39, v39, v39 row_bcast:15 row_mask:0xa bank_mask:0xf
	s_nop 1
	v_add_u32_dpp v39, v39, v39 row_bcast:31 row_mask:0xc bank_mask:0xf
	v_lshrrev_b32_e32 v40, 6, v0
	s_nop 0
	v_readfirstlane_b32 s3, v40
	v_readlane_b32 s14, v39, 63
	s_lshl_b32 s15, s3, 2
	s_add_u32 s15, s15, 0x2400
	v_mov_b32_e32 v41, s14
	v_mov_b32_e32 v42, s15
	s_mov_b64 s[38:39], exec
	s_mov_b64 exec, 1
	ds_write_b32 v42, v41
	s_mov_b64 exec, s[38:39]
	s_waitcnt lgkmcnt(0)
	s_barrier
	v_and_b32_e32 v41, 15, v0
	v_lshlrev_b32_e32 v41, 2, v41
	ds_read_b32 v41, v41 offset:9216
	s_waitcnt lgkmcnt(0)
	s_nop 1
	v_add_u32_dpp v41, v41, v41 row_shr:1 row_mask:0xf bank_mask:0xf bound_ctrl:0
	s_nop 1
	v_add_u32_dpp v41, v41, v41 row_shr:2 row_mask:0xf bank_mask:0xf bound_ctrl:0
	s_nop 1
	v_add_u32_dpp v41, v41, v41 row_shr:4 row_mask:0xf bank_mask:0xf bound_ctrl:0
	s_nop 1
	v_add_u32_dpp v41, v41, v41 row_shr:8 row_mask:0xf bank_mask:0xf bound_ctrl:0
	s_sub_u32 s15, s3, 1
	s_max_i32 s15, s15, 0
	s_nop 1
	v_readlane_b32 s16, v41, s15
	s_cmp_eq_u32 s3, 0
	s_cselect_b32 s16, 0, s16
	v_sub_u32_e32 v43, v39, v38
	v_add_u32_e32 v43, s16, v43
	v_add_u32_e32 v47, v43, v34
	v_add_u32_e32 v44, v43, v36
	v_add_u32_e32 v45, v47, v37
	v_mov_b32_e32 v46, v43
	v_mov_b32_e32 v48, 0
	v_mov_b32_e32 v49, 0
	v_lshlrev_b32_e32 v42, 3, v0
	v_cmp_gt_u32_e32 vcc, 0x224, v0
	s_and_saveexec_b64 s[36:37], vcc
	ds_write_b64 v42, v[44:45]
	ds_write_b64 v42, v[48:49] offset:4608
	s_cmp_lg_u32 s2, 0
	s_cbranch_scc1 .Lsc_nobb
	s_cbranch_execz .Lsc_nobb
	global_store_dwordx2 v42, v[46:47], s[12:13]
.Lsc_nobb:
	s_mov_b64 exec, s[36:37]
	s_waitcnt lgkmcnt(0)
	s_barrier
	v_mov_b32_e32 v50, 1
	v_mov_b32_e32 v60, 0x447
	v_mov_b32_e32 v61, 0x1200
	s_cmp_ge_u32 0, s26
	s_cbranch_scc0 .Lsc_dskip0
	s_cmp_lt_u32 0, s27
	s_cbranch_scc0 .Lsc_dskip0
	v_cmp_gt_i32_e64 s[20:21], 0, v3
	v_subrev_co_u32_e32 v51, vcc, 0x61a80, v3
	v_lshrrev_b32_e32 v51, 6, v51
	v_lshrrev_b32_e32 v52, 9, v3
	v_add_u32_e32 v51, 0x30e, v51
	v_cndmask_b32_e32 v51, v51, v52, vcc
	v_cndmask_b32_e64 v51, v51, v60, s[20:21]
	v_lshl_add_u32 v34, v51, 2, v61
	ds_add_rtn_u32 v34, v34, v50
.Lsc_dskip0:
	s_cmp_ge_u32 1, s26
	s_cbranch_scc0 .Lsc_dskip1
	s_cmp_lt_u32 1, s27
	s_cbranch_scc0 .Lsc_dskip1
	v_cmp_gt_i32_e64 s[20:21], 0, v5
	v_subrev_co_u32_e32 v51, vcc, 0x61a80, v5
	v_lshrrev_b32_e32 v51, 6, v51
	v_lshrrev_b32_e32 v52, 9, v5
	v_add_u32_e32 v51, 0x30e, v51
	v_cndmask_b32_e32 v51, v51, v52, vcc
	v_cndmask_b32_e64 v51, v51, v60, s[20:21]
	v_lshl_add_u32 v35, v51, 2, v61
	ds_add_rtn_u32 v35, v35, v50
.Lsc_dskip1:
	s_cmp_ge_u32 2, s26
	s_cbranch_scc0 .Lsc_dskip2
	s_cmp_lt_u32 2, s27
	s_cbranch_scc0 .Lsc_dskip2
	v_cmp_gt_i32_e64 s[20:21], 0, v7
	v_subrev_co_u32_e32 v51, vcc, 0x61a80, v7
	v_lshrrev_b32_e32 v51, 6, v51
	v_lshrrev_b32_e32 v52, 9, v7
	v_add_u32_e32 v51, 0x30e, v51
	v_cndmask_b32_e32 v51, v51, v52, vcc
	v_cndmask_b32_e64 v51, v51, v60, s[20:21]
	v_lshl_add_u32 v36, v51, 2, v61
	ds_add_rtn_u32 v36, v36, v50
.Lsc_dskip2:
	s_cmp_ge_u32 3, s26
	s_cbranch_scc0 .Lsc_dskip3
	s_cmp_lt_u32 3, s27
	s_cbranch_scc0 .Lsc_dskip3
	v_cmp_gt_i32_e64 s[20:21], 0, v9
	v_subrev_co_u32_e32 v51, vcc, 0x61a80, v9
	v_lshrrev_b32_e32 v51, 6, v51
	v_lshrrev_b32_e32 v52, 9, v9
	v_add_u32_e32 v51, 0x30e, v51
	v_cndmask_b32_e32 v51, v51, v52, vcc
	v_cndmask_b32_e64 v51, v51, v60, s[20:21]
	v_lshl_add_u32 v37, v51, 2, v61
	ds_add_rtn_u32 v37, v37, v50
.Lsc_dskip3:
	s_cmp_ge_u32 4, s26
	s_cbranch_scc0 .Lsc_dskip4
	s_cmp_lt_u32 4, s27
	s_cbranch_scc0 .Lsc_dskip4
	v_cmp_gt_i32_e64 s[20:21], 0, v11
	v_subrev_co_u32_e32 v51, vcc, 0x61a80, v11
	v_lshrrev_b32_e32 v51, 6, v51
	v_lshrrev_b32_e32 v52, 9, v11
	v_add_u32_e32 v51, 0x30e, v51
	v_cndmask_b32_e32 v51, v51, v52, vcc
	v_cndmask_b32_e64 v51, v51, v60, s[20:21]
	v_lshl_add_u32 v38, v51, 2, v61
	ds_add_rtn_u32 v38, v38, v50
.Lsc_dskip4:
	s_cmp_ge_u32 5, s26
	s_cbranch_scc0 .Lsc_dskip5
	s_cmp_lt_u32 5, s27
	s_cbranch_scc0 .Lsc_dskip5
	v_cmp_gt_i32_e64 s[20:21], 0, v13
	v_subrev_co_u32_e32 v51, vcc, 0x61a80, v13
	v_lshrrev_b32_e32 v51, 6, v51
	v_lshrrev_b32_e32 v52, 9, v13
	v_add_u32_e32 v51, 0x30e, v51
	v_cndmask_b32_e32 v51, v51, v52, vcc
	v_cndmask_b32_e64 v51, v51, v60, s[20:21]
	v_lshl_add_u32 v39, v51, 2, v61
	ds_add_rtn_u32 v39, v39, v50
.Lsc_dskip5:
	s_cmp_ge_u32 6, s26
	s_cbranch_scc0 .Lsc_dskip6
	s_cmp_lt_u32 6, s27
	s_cbranch_scc0 .Lsc_dskip6
	v_cmp_gt_i32_e64 s[20:21], 0, v15
	v_subrev_co_u32_e32 v51, vcc, 0x61a80, v15
	v_lshrrev_b32_e32 v51, 6, v51
	v_lshrrev_b32_e32 v52, 9, v15
	v_add_u32_e32 v51, 0x30e, v51
	v_cndmask_b32_e32 v51, v51, v52, vcc
	v_cndmask_b32_e64 v51, v51, v60, s[20:21]
	v_lshl_add_u32 v40, v51, 2, v61
	ds_add_rtn_u32 v40, v40, v50
.Lsc_dskip6:
	s_cmp_ge_u32 7, s26
	s_cbranch_scc0 .Lsc_dskip7
	s_cmp_lt_u32 7, s27
	s_cbranch_scc0 .Lsc_dskip7
	v_cmp_gt_i32_e64 s[20:21], 0, v17
	v_subrev_co_u32_e32 v51, vcc, 0x61a80, v17
	v_lshrrev_b32_e32 v51, 6, v51
	v_lshrrev_b32_e32 v52, 9, v17
	v_add_u32_e32 v51, 0x30e, v51
	v_cndmask_b32_e32 v51, v51, v52, vcc
	v_cndmask_b32_e64 v51, v51, v60, s[20:21]
	v_lshl_add_u32 v41, v51, 2, v61
	ds_add_rtn_u32 v41, v41, v50
.Lsc_dskip7:
	s_cmp_ge_u32 8, s26
	s_cbranch_scc0 .Lsc_dskip8
	s_cmp_lt_u32 8, s27
	s_cbranch_scc0 .Lsc_dskip8
	v_cmp_gt_i32_e64 s[20:21], 0, v19
	v_subrev_co_u32_e32 v51, vcc, 0x61a80, v19
	v_lshrrev_b32_e32 v51, 6, v51
	v_lshrrev_b32_e32 v52, 9, v19
	v_add_u32_e32 v51, 0x30e, v51
	v_cndmask_b32_e32 v51, v51, v52, vcc
	v_cndmask_b32_e64 v51, v51, v60, s[20:21]
	v_lshl_add_u32 v42, v51, 2, v61
	ds_add_rtn_u32 v42, v42, v50
.Lsc_dskip8:
	s_cmp_ge_u32 9, s26
	s_cbranch_scc0 .Lsc_dskip9
	s_cmp_lt_u32 9, s27
	s_cbranch_scc0 .Lsc_dskip9
	v_cmp_gt_i32_e64 s[20:21], 0, v21
	v_subrev_co_u32_e32 v51, vcc, 0x61a80, v21
	v_lshrrev_b32_e32 v51, 6, v51
	v_lshrrev_b32_e32 v52, 9, v21
	v_add_u32_e32 v51, 0x30e, v51
	v_cndmask_b32_e32 v51, v51, v52, vcc
	v_cndmask_b32_e64 v51, v51, v60, s[20:21]
	v_lshl_add_u32 v43, v51, 2, v61
	ds_add_rtn_u32 v43, v43, v50
.Lsc_dskip9:
	s_cmp_ge_u32 10, s26
	s_cbranch_scc0 .Lsc_dskip10
	s_cmp_lt_u32 10, s27
	s_cbranch_scc0 .Lsc_dskip10
	v_cmp_gt_i32_e64 s[20:21], 0, v23
	v_subrev_co_u32_e32 v51, vcc, 0x61a80, v23
	v_lshrrev_b32_e32 v51, 6, v51
	v_lshrrev_b32_e32 v52, 9, v23
	v_add_u32_e32 v51, 0x30e, v51
	v_cndmask_b32_e32 v51, v51, v52, vcc
	v_cndmask_b32_e64 v51, v51, v60, s[20:21]
	v_lshl_add_u32 v44, v51, 2, v61
	ds_add_rtn_u32 v44, v44, v50
.Lsc_dskip10:
	s_cmp_ge_u32 11, s26
	s_cbranch_scc0 .Lsc_dskip11
	s_cmp_lt_u32 11, s27
	s_cbranch_scc0 .Lsc_dskip11
	v_cmp_gt_i32_e64 s[20:21], 0, v25
	v_subrev_co_u32_e32 v51, vcc, 0x61a80, v25
	v_lshrrev_b32_e32 v51, 6, v51
	v_lshrrev_b32_e32 v52, 9, v25
	v_add_u32_e32 v51, 0x30e, v51
	v_cndmask_b32_e32 v51, v51, v52, vcc
	v_cndmask_b32_e64 v51, v51, v60, s[20:21]
	v_lshl_add_u32 v45, v51, 2, v61
	ds_add_rtn_u32 v45, v45, v50
.Lsc_dskip11:
	s_cmp_ge_u32 12, s26
	s_cbranch_scc0 .Lsc_dskip12
	s_cmp_lt_u32 12, s27
	s_cbranch_scc0 .Lsc_dskip12
	v_cmp_gt_i32_e64 s[20:21], 0, v27
	v_subrev_co_u32_e32 v51, vcc, 0x61a80, v27
	v_lshrrev_b32_e32 v51, 6, v51
	v_lshrrev_b32_e32 v52, 9, v27
	v_add_u32_e32 v51, 0x30e, v51
	v_cndmask_b32_e32 v51, v51, v52, vcc
	v_cndmask_b32_e64 v51, v51, v60, s[20:21]
	v_lshl_add_u32 v46, v51, 2, v61
	ds_add_rtn_u32 v46, v46, v50
.Lsc_dskip12:
	s_cmp_ge_u32 13, s26
	s_cbranch_scc0 .Lsc_dskip13
	s_cmp_lt_u32 13, s27
	s_cbranch_scc0 .Lsc_dskip13
	v_cmp_gt_i32_e64 s[20:21], 0, v29
	v_subrev_co_u32_e32 v51, vcc, 0x61a80, v29
	v_lshrrev_b32_e32 v51, 6, v51
	v_lshrrev_b32_e32 v52, 9, v29
	v_add_u32_e32 v51, 0x30e, v51
	v_cndmask_b32_e32 v51, v51, v52, vcc
	v_cndmask_b32_e64 v51, v51, v60, s[20:21]
	v_lshl_add_u32 v47, v51, 2, v61
	ds_add_rtn_u32 v47, v47, v50
.Lsc_dskip13:
	s_cmp_ge_u32 14, s26
	s_cbranch_scc0 .Lsc_dskip14
	s_cmp_lt_u32 14, s27
	s_cbranch_scc0 .Lsc_dskip14
	v_cmp_gt_i32_e64 s[20:21], 0, v31
	v_subrev_co_u32_e32 v51, vcc, 0x61a80, v31
	v_lshrrev_b32_e32 v51, 6, v51
	v_lshrrev_b32_e32 v52, 9, v31
	v_add_u32_e32 v51, 0x30e, v51
	v_cndmask_b32_e32 v51, v51, v52, vcc
	v_cndmask_b32_e64 v51, v51, v60, s[20:21]
	v_lshl_add_u32 v48, v51, 2, v61
	ds_add_rtn_u32 v48, v48, v50
.Lsc_dskip14:
	s_cmp_ge_u32 15, s26
	s_cbranch_scc0 .Lsc_dskip15
	s_cmp_lt_u32 15, s27
	s_cbranch_scc0 .Lsc_dskip15
	v_cmp_gt_i32_e64 s[20:21], 0, v33
	v_subrev_co_u32_e32 v51, vcc, 0x61a80, v33
	v_lshrrev_b32_e32 v51, 6, v51
	v_lshrrev_b32_e32 v52, 9, v33
	v_add_u32_e32 v51, 0x30e, v51
	v_cndmask_b32_e32 v51, v51, v52, vcc
	v_cndmask_b32_e64 v51, v51, v60, s[20:21]
	v_lshl_add_u32 v49, v51, 2, v61
	ds_add_rtn_u32 v49, v49, v50
.Lsc_dskip15:
	s_waitcnt lgkmcnt(0)
	s_barrier
	v_lshlrev_b32_e32 v50, 3, v0
	v_mov_b32_e32 v52, 0
	v_mov_b32_e32 v53, 0
	v_cmp_gt_u32_e32 vcc, 0x224, v0
	s_and_saveexec_b64 s[36:37], vcc
	ds_read_b64 v[52:53], v50 offset:4608
	s_mov_b64 exec, s[36:37]
	s_waitcnt lgkmcnt(0)
	v_add_u32_e32 v54, v52, v53
	v_mov_b32_e32 v55, v54
	s_nop 1
	v_add_u32_dpp v55, v55, v55 row_shr:1 row_mask:0xf bank_mask:0xf bound_ctrl:0
	s_nop 1
	v_add_u32_dpp v55, v55, v55 row_shr:2 row_mask:0xf bank_mask:0xf bound_ctrl:0
	s_nop 1
	v_add_u32_dpp v55, v55, v55 row_shr:4 row_mask:0xf bank_mask:0xf bound_ctrl:0
	s_nop 1
	v_add_u32_dpp v55, v55, v55 row_shr:8 row_mask:0xf bank_mask:0xf bound_ctrl:0
	s_nop 1
	v_add_u32_dpp v55, v55, v55 row_bcast:15 row_mask:0xa bank_mask:0xf
	s_nop 1
	v_add_u32_dpp v55, v55, v55 row_bcast:31 row_mask:0xc bank_mask:0xf
	v_lshrrev_b32_e32 v56, 6, v0
	s_nop 0
	v_readfirstlane_b32 s3, v56
	v_readlane_b32 s14, v55, 63
	s_lshl_b32 s15, s3, 2
	s_add_u32 s15, s15, 0x2400
	v_mov_b32_e32 v57, s14
	v_mov_b32_e32 v58, s15
	s_mov_b64 s[38:39], exec
	s_mov_b64 exec, 1
	ds_write_b32 v58, v57
	s_mov_b64 exec, s[38:39]
	s_waitcnt lgkmcnt(0)
	s_barrier
	v_and_b32_e32 v57, 15, v0
	v_lshlrev_b32_e32 v57, 2, v57
	ds_read_b32 v57, v57 offset:9216
	s_waitcnt lgkmcnt(0)
	s_nop 1
	v_add_u32_dpp v57, v57, v57 row_shr:1 row_mask:0xf bank_mask:0xf bound_ctrl:0
	s_nop 1
	v_add_u32_dpp v57, v57, v57 row_shr:2 row_mask:0xf bank_mask:0xf bound_ctrl:0
	s_nop 1
	v_add_u32_dpp v57, v57, v57 row_shr:4 row_mask:0xf bank_mask:0xf bound_ctrl:0
	s_nop 1
	v_add_u32_dpp v57, v57, v57 row_shr:8 row_mask:0xf bank_mask:0xf bound_ctrl:0
	s_sub_u32 s15, s3, 1
	s_max_i32 s15, s15, 0
	s_nop 1
	v_readlane_b32 s16, v57, s15
	s_cmp_eq_u32 s3, 0
	s_cselect_b32 s16, 0, s16
	v_sub_u32_e32 v58, v55, v54
	v_add_u32_e32 v58, s16, v58
	v_add_u32_e32 v59, v58, v52
	v_cmp_gt_u32_e32 vcc, 0x224, v0
	s_and_saveexec_b64 s[36:37], vcc
	ds_read_b64 v[56:57], v50
	ds_write_b64 v50, v[58:59] offset:9728
	s_waitcnt lgkmcnt(0)
	v_sub_u32_e32 v56, v56, v58
	v_sub_u32_e32 v57, v57, v59
	ds_write_b64 v50, v[56:57]
	s_mov_b64 exec, s[36:37]
	s_waitcnt lgkmcnt(0)
	s_barrier
	v_mov_b32_e32 v60, 0x447
	v_cmp_gt_i32_e64 s[20:21], 0, v3
	v_subrev_co_u32_e32 v51, vcc, 0x61a80, v3
	v_lshrrev_b32_e32 v51, 6, v51
	v_lshrrev_b32_e32 v52, 9, v3
	v_add_u32_e32 v51, 0x30e, v51
	v_cndmask_b32_e32 v51, v51, v52, vcc
	v_cndmask_b32_e64 v51, v51, v60, s[20:21]
	v_lshlrev_b32_e32 v51, 2, v51
	ds_read_b32 v53, v51 offset:9728
	v_cmp_gt_i32_e64 s[20:21], 0, v5
	v_subrev_co_u32_e32 v51, vcc, 0x61a80, v5
	v_lshrrev_b32_e32 v51, 6, v51
	v_lshrrev_b32_e32 v52, 9, v5
	v_add_u32_e32 v51, 0x30e, v51
	v_cndmask_b32_e32 v51, v51, v52, vcc
	v_cndmask_b32_e64 v51, v51, v60, s[20:21]
	v_lshlrev_b32_e32 v51, 2, v51
	ds_read_b32 v54, v51 offset:9728
	v_cmp_gt_i32_e64 s[20:21], 0, v7
	v_subrev_co_u32_e32 v51, vcc, 0x61a80, v7
	v_lshrrev_b32_e32 v51, 6, v51
	v_lshrrev_b32_e32 v52, 9, v7
	v_add_u32_e32 v51, 0x30e, v51
	v_cndmask_b32_e32 v51, v51, v52, vcc
	v_cndmask_b32_e64 v51, v51, v60, s[20:21]
	v_lshlrev_b32_e32 v51, 2, v51
	ds_read_b32 v55, v51 offset:9728
	v_cmp_gt_i32_e64 s[20:21], 0, v9
	v_subrev_co_u32_e32 v51, vcc, 0x61a80, v9
	v_lshrrev_b32_e32 v51, 6, v51
	v_lshrrev_b32_e32 v52, 9, v9
	v_add_u32_e32 v51, 0x30e, v51
	v_cndmask_b32_e32 v51, v51, v52, vcc
	v_cndmask_b32_e64 v51, v51, v60, s[20:21]
	v_lshlrev_b32_e32 v51, 2, v51
	ds_read_b32 v56, v51 offset:9728
	s_waitcnt lgkmcnt(0)
	v_add_u32_e32 v34, v34, v53
	v_add_u32_e32 v35, v35, v54
	v_add_u32_e32 v36, v36, v55
	v_add_u32_e32 v37, v37, v56
	v_cmp_gt_i32_e64 s[20:21], 0, v11
	v_subrev_co_u32_e32 v51, vcc, 0x61a80, v11
	v_lshrrev_b32_e32 v51, 6, v51
	v_lshrrev_b32_e32 v52, 9, v11
	v_add_u32_e32 v51, 0x30e, v51
	v_cndmask_b32_e32 v51, v51, v52, vcc
	v_cndmask_b32_e64 v51, v51, v60, s[20:21]
	v_lshlrev_b32_e32 v51, 2, v51
	ds_read_b32 v53, v51 offset:9728
	v_cmp_gt_i32_e64 s[20:21], 0, v13
	v_subrev_co_u32_e32 v51, vcc, 0x61a80, v13
	v_lshrrev_b32_e32 v51, 6, v51
	v_lshrrev_b32_e32 v52, 9, v13
	v_add_u32_e32 v51, 0x30e, v51
	v_cndmask_b32_e32 v51, v51, v52, vcc
	v_cndmask_b32_e64 v51, v51, v60, s[20:21]
	v_lshlrev_b32_e32 v51, 2, v51
	ds_read_b32 v54, v51 offset:9728
	v_cmp_gt_i32_e64 s[20:21], 0, v15
	v_subrev_co_u32_e32 v51, vcc, 0x61a80, v15
	v_lshrrev_b32_e32 v51, 6, v51
	v_lshrrev_b32_e32 v52, 9, v15
	v_add_u32_e32 v51, 0x30e, v51
	v_cndmask_b32_e32 v51, v51, v52, vcc
	v_cndmask_b32_e64 v51, v51, v60, s[20:21]
	v_lshlrev_b32_e32 v51, 2, v51
	ds_read_b32 v55, v51 offset:9728
	v_cmp_gt_i32_e64 s[20:21], 0, v17
	v_subrev_co_u32_e32 v51, vcc, 0x61a80, v17
	v_lshrrev_b32_e32 v51, 6, v51
	v_lshrrev_b32_e32 v52, 9, v17
	v_add_u32_e32 v51, 0x30e, v51
	v_cndmask_b32_e32 v51, v51, v52, vcc
	v_cndmask_b32_e64 v51, v51, v60, s[20:21]
	v_lshlrev_b32_e32 v51, 2, v51
	ds_read_b32 v56, v51 offset:9728
	s_waitcnt lgkmcnt(0)
	v_add_u32_e32 v38, v38, v53
	v_add_u32_e32 v39, v39, v54
	v_add_u32_e32 v40, v40, v55
	v_add_u32_e32 v41, v41, v56
	v_cmp_gt_i32_e64 s[20:21], 0, v19
	v_subrev_co_u32_e32 v51, vcc, 0x61a80, v19
	v_lshrrev_b32_e32 v51, 6, v51
	v_lshrrev_b32_e32 v52, 9, v19
	v_add_u32_e32 v51, 0x30e, v51
	v_cndmask_b32_e32 v51, v51, v52, vcc
	v_cndmask_b32_e64 v51, v51, v60, s[20:21]
	v_lshlrev_b32_e32 v51, 2, v51
	ds_read_b32 v53, v51 offset:9728
	v_cmp_gt_i32_e64 s[20:21], 0, v21
	v_subrev_co_u32_e32 v51, vcc, 0x61a80, v21
	v_lshrrev_b32_e32 v51, 6, v51
	v_lshrrev_b32_e32 v52, 9, v21
	v_add_u32_e32 v51, 0x30e, v51
	v_cndmask_b32_e32 v51, v51, v52, vcc
	v_cndmask_b32_e64 v51, v51, v60, s[20:21]
	v_lshlrev_b32_e32 v51, 2, v51
	ds_read_b32 v54, v51 offset:9728
	v_cmp_gt_i32_e64 s[20:21], 0, v23
	v_subrev_co_u32_e32 v51, vcc, 0x61a80, v23
	v_lshrrev_b32_e32 v51, 6, v51
	v_lshrrev_b32_e32 v52, 9, v23
	v_add_u32_e32 v51, 0x30e, v51
	v_cndmask_b32_e32 v51, v51, v52, vcc
	v_cndmask_b32_e64 v51, v51, v60, s[20:21]
	v_lshlrev_b32_e32 v51, 2, v51
	ds_read_b32 v55, v51 offset:9728
	v_cmp_gt_i32_e64 s[20:21], 0, v25
	v_subrev_co_u32_e32 v51, vcc, 0x61a80, v25
	v_lshrrev_b32_e32 v51, 6, v51
	v_lshrrev_b32_e32 v52, 9, v25
	v_add_u32_e32 v51, 0x30e, v51
	v_cndmask_b32_e32 v51, v51, v52, vcc
	v_cndmask_b32_e64 v51, v51, v60, s[20:21]
	v_lshlrev_b32_e32 v51, 2, v51
	ds_read_b32 v56, v51 offset:9728
	s_waitcnt lgkmcnt(0)
	v_add_u32_e32 v42, v42, v53
	v_add_u32_e32 v43, v43, v54
	v_add_u32_e32 v44, v44, v55
	v_add_u32_e32 v45, v45, v56
	v_cmp_gt_i32_e64 s[20:21], 0, v27
	v_subrev_co_u32_e32 v51, vcc, 0x61a80, v27
	v_lshrrev_b32_e32 v51, 6, v51
	v_lshrrev_b32_e32 v52, 9, v27
	v_add_u32_e32 v51, 0x30e, v51
	v_cndmask_b32_e32 v51, v51, v52, vcc
	v_cndmask_b32_e64 v51, v51, v60, s[20:21]
	v_lshlrev_b32_e32 v51, 2, v51
	ds_read_b32 v53, v51 offset:9728
	v_cmp_gt_i32_e64 s[20:21], 0, v29
	v_subrev_co_u32_e32 v51, vcc, 0x61a80, v29
	v_lshrrev_b32_e32 v51, 6, v51
	v_lshrrev_b32_e32 v52, 9, v29
	v_add_u32_e32 v51, 0x30e, v51
	v_cndmask_b32_e32 v51, v51, v52, vcc
	v_cndmask_b32_e64 v51, v51, v60, s[20:21]
	v_lshlrev_b32_e32 v51, 2, v51
	ds_read_b32 v54, v51 offset:9728
	v_cmp_gt_i32_e64 s[20:21], 0, v31
	v_subrev_co_u32_e32 v51, vcc, 0x61a80, v31
	v_lshrrev_b32_e32 v51, 6, v51
	v_lshrrev_b32_e32 v52, 9, v31
	v_add_u32_e32 v51, 0x30e, v51
	v_cndmask_b32_e32 v51, v51, v52, vcc
	v_cndmask_b32_e64 v51, v51, v60, s[20:21]
	v_lshlrev_b32_e32 v51, 2, v51
	ds_read_b32 v55, v51 offset:9728
	v_cmp_gt_i32_e64 s[20:21], 0, v33
	v_subrev_co_u32_e32 v51, vcc, 0x61a80, v33
	v_lshrrev_b32_e32 v51, 6, v51
	v_lshrrev_b32_e32 v52, 9, v33
	v_add_u32_e32 v51, 0x30e, v51
	v_cndmask_b32_e32 v51, v51, v52, vcc
	v_cndmask_b32_e64 v51, v51, v60, s[20:21]
	v_lshlrev_b32_e32 v51, 2, v51
	ds_read_b32 v56, v51 offset:9728
	s_waitcnt lgkmcnt(0)
	v_add_u32_e32 v46, v46, v53
	v_add_u32_e32 v47, v47, v54
	v_add_u32_e32 v48, v48, v55
	v_add_u32_e32 v49, v49, v56
	s_mov_b64 s[38:39], exec
	s_movk_i32 s14, 0x1000
	v_cmp_gt_u32_e32 vcc, s14, v34
	v_lshlrev_b32_e32 v52, 3, v34
	s_and_b64 exec, s[38:39], vcc
	ds_write_b64 v52, v[2:3] offset:14336
	s_mov_b64 exec, s[38:39]
	v_cmp_gt_u32_e32 vcc, s14, v35
	v_lshlrev_b32_e32 v52, 3, v35
	s_and_b64 exec, s[38:39], vcc
	ds_write_b64 v52, v[4:5] offset:14336
	s_mov_b64 exec, s[38:39]
	v_cmp_gt_u32_e32 vcc, s14, v36
	v_lshlrev_b32_e32 v52, 3, v36
	s_and_b64 exec, s[38:39], vcc
	ds_write_b64 v52, v[6:7] offset:14336
	s_mov_b64 exec, s[38:39]
	v_cmp_gt_u32_e32 vcc, s14, v37
	v_lshlrev_b32_e32 v52, 3, v37
	s_and_b64 exec, s[38:39], vcc
	ds_write_b64 v52, v[8:9] offset:14336
	s_mov_b64 exec, s[38:39]
	v_cmp_gt_u32_e32 vcc, s14, v38
	v_lshlrev_b32_e32 v52, 3, v38
	s_and_b64 exec, s[38:39], vcc
	ds_write_b64 v52, v[10:11] offset:14336
	s_mov_b64 exec, s[38:39]
	v_cmp_gt_u32_e32 vcc, s14, v39
	v_lshlrev_b32_e32 v52, 3, v39
	s_and_b64 exec, s[38:39], vcc
	ds_write_b64 v52, v[12:13] offset:14336
	s_mov_b64 exec, s[38:39]
	v_cmp_gt_u32_e32 vcc, s14, v40
	v_lshlrev_b32_e32 v52, 3, v40
	s_and_b64 exec, s[38:39], vcc
	ds_write_b64 v52, v[14:15] offset:14336
	s_mov_b64 exec, s[38:39]
	v_cmp_gt_u32_e32 vcc, s14, v41
	v_lshlrev_b32_e32 v52, 3, v41
	s_and_b64 exec, s[38:39], vcc
	ds_write_b64 v52, v[16:17] offset:14336
	s_mov_b64 exec, s[38:39]
	v_cmp_gt_u32_e32 vcc, s14, v42
	v_lshlrev_b32_e32 v52, 3, v42
	s_and_b64 exec, s[38:39], vcc
	ds_write_b64 v52, v[18:19] offset:14336
	s_mov_b64 exec, s[38:39]
	v_cmp_gt_u32_e32 vcc, s14, v43
	v_lshlrev_b32_e32 v52, 3, v43
	s_and_b64 exec, s[38:39], vcc
	ds_write_b64 v52, v[20:21] offset:14336
	s_mov_b64 exec, s[38:39]
	v_cmp_gt_u32_e32 vcc, s14, v44
	v_lshlrev_b32_e32 v52, 3, v44
	s_and_b64 exec, s[38:39], vcc
	ds_write_b64 v52, v[22:23] offset:14336
	s_mov_b64 exec, s[38:39]
	v_cmp_gt_u32_e32 vcc, s14, v45
	v_lshlrev_b32_e32 v52, 3, v45
	s_and_b64 exec, s[38:39], vcc
	ds_write_b64 v52, v[24:25] offset:14336
	s_mov_b64 exec, s[38:39]
	v_cmp_gt_u32_e32 vcc, s14, v46
	v_lshlrev_b32_e32 v52, 3, v46
	s_and_b64 exec, s[38:39], vcc
	ds_write_b64 v52, v[26:27] offset:14336
	s_mov_b64 exec, s[38:39]
	v_cmp_gt_u32_e32 vcc, s14, v47
	v_lshlrev_b32_e32 v52, 3, v47
	s_and_b64 exec, s[38:39], vcc
	ds_write_b64 v52, v[28:29] offset:14336
	s_mov_b64 exec, s[38:39]
	v_cmp_gt_u32_e32 vcc, s14, v48
	v_lshlrev_b32_e32 v52, 3, v48
	s_and_b64 exec, s[38:39], vcc
	ds_write_b64 v52, v[30:31] offset:14336
	s_mov_b64 exec, s[38:39]
	v_cmp_gt_u32_e32 vcc, s14, v49
	v_lshlrev_b32_e32 v52, 3, v49
	s_and_b64 exec, s[38:39], vcc
	ds_write_b64 v52, v[32:33] offset:14336
	s_mov_b64 exec, s[38:39]
	s_waitcnt lgkmcnt(0)
	s_barrier
	v_mov_b32_e32 v61, v0
	v_lshlrev_b32_e32 v62, 3, v61
	ds_read_b64 v[50:51], v62 offset:14336
	s_waitcnt lgkmcnt(0)
	v_subrev_co_u32_e32 v53, vcc, 0x61a80, v51
	v_lshrrev_b32_e32 v53, 6, v53
	v_lshrrev_b32_e32 v54, 9, v51
	v_add_u32_e32 v53, 0x30e, v53
	v_cndmask_b32_e32 v53, v53, v54, vcc
	v_min_u32_e32 v53, 0x447, v53
	v_lshlrev_b32_e32 v53, 2, v53
	ds_read_b32 v53, v53
	v_cmp_le_i32_e32 vcc, 0, v51
	s_waitcnt lgkmcnt(0)
	v_add_u32_e32 v53, v53, v61
	v_lshlrev_b32_e32 v53, 3, v53
	s_and_b64 exec, s[38:39], vcc
	global_store_dwordx2 v53, v[50:51], s[34:35]
	s_mov_b64 exec, s[38:39]
	v_add_u32_e32 v61, 0x400, v0
	v_lshlrev_b32_e32 v62, 3, v61
	ds_read_b64 v[50:51], v62 offset:14336
	s_waitcnt lgkmcnt(0)
	v_subrev_co_u32_e32 v53, vcc, 0x61a80, v51
	v_lshrrev_b32_e32 v53, 6, v53
	v_lshrrev_b32_e32 v54, 9, v51
	v_add_u32_e32 v53, 0x30e, v53
	v_cndmask_b32_e32 v53, v53, v54, vcc
	v_min_u32_e32 v53, 0x447, v53
	v_lshlrev_b32_e32 v53, 2, v53
	ds_read_b32 v53, v53
	v_cmp_le_i32_e32 vcc, 0, v51
	s_waitcnt lgkmcnt(0)
	v_add_u32_e32 v53, v53, v61
	v_lshlrev_b32_e32 v53, 3, v53
	s_and_b64 exec, s[38:39], vcc
	global_store_dwordx2 v53, v[50:51], s[34:35]
	s_mov_b64 exec, s[38:39]
	v_add_u32_e32 v61, 0x800, v0
	v_lshlrev_b32_e32 v62, 3, v61
	ds_read_b64 v[50:51], v62 offset:14336
	s_waitcnt lgkmcnt(0)
	v_subrev_co_u32_e32 v53, vcc, 0x61a80, v51
	v_lshrrev_b32_e32 v53, 6, v53
	v_lshrrev_b32_e32 v54, 9, v51
	v_add_u32_e32 v53, 0x30e, v53
	v_cndmask_b32_e32 v53, v53, v54, vcc
	v_min_u32_e32 v53, 0x447, v53
	v_lshlrev_b32_e32 v53, 2, v53
	ds_read_b32 v53, v53
	v_cmp_le_i32_e32 vcc, 0, v51
	s_waitcnt lgkmcnt(0)
	v_add_u32_e32 v53, v53, v61
	v_lshlrev_b32_e32 v53, 3, v53
	s_and_b64 exec, s[38:39], vcc
	global_store_dwordx2 v53, v[50:51], s[34:35]
	s_mov_b64 exec, s[38:39]
	v_add_u32_e32 v61, 0xc00, v0
	v_lshlrev_b32_e32 v62, 3, v61
	ds_read_b64 v[50:51], v62 offset:14336
	s_waitcnt lgkmcnt(0)
	v_subrev_co_u32_e32 v53, vcc, 0x61a80, v51
	v_lshrrev_b32_e32 v53, 6, v53
	v_lshrrev_b32_e32 v54, 9, v51
	v_add_u32_e32 v53, 0x30e, v53
	v_cndmask_b32_e32 v53, v53, v54, vcc
	v_min_u32_e32 v53, 0x447, v53
	v_lshlrev_b32_e32 v53, 2, v53
	ds_read_b32 v53, v53
	v_cmp_le_i32_e32 vcc, 0, v51
	s_waitcnt lgkmcnt(0)
	v_add_u32_e32 v53, v53, v61
	v_lshlrev_b32_e32 v53, 3, v53
	s_and_b64 exec, s[38:39], vcc
	global_store_dwordx2 v53, v[50:51], s[34:35]
	s_mov_b64 exec, s[38:39]
	s_barrier
	v_subrev_u32_e32 v51, 0x1000, v34
	v_cmp_gt_u32_e32 vcc, s14, v51
	v_lshlrev_b32_e32 v52, 3, v51
	s_and_b64 exec, s[38:39], vcc
	ds_write_b64 v52, v[2:3] offset:14336
	s_mov_b64 exec, s[38:39]
	v_subrev_u32_e32 v51, 0x1000, v35
	v_cmp_gt_u32_e32 vcc, s14, v51
	v_lshlrev_b32_e32 v52, 3, v51
	s_and_b64 exec, s[38:39], vcc
	ds_write_b64 v52, v[4:5] offset:14336
	s_mov_b64 exec, s[38:39]
	v_subrev_u32_e32 v51, 0x1000, v36
	v_cmp_gt_u32_e32 vcc, s14, v51
	v_lshlrev_b32_e32 v52, 3, v51
	s_and_b64 exec, s[38:39], vcc
	ds_write_b64 v52, v[6:7] offset:14336
	s_mov_b64 exec, s[38:39]
	v_subrev_u32_e32 v51, 0x1000, v37
	v_cmp_gt_u32_e32 vcc, s14, v51
	v_lshlrev_b32_e32 v52, 3, v51
	s_and_b64 exec, s[38:39], vcc
	ds_write_b64 v52, v[8:9] offset:14336
	s_mov_b64 exec, s[38:39]
	v_subrev_u32_e32 v51, 0x1000, v38
	v_cmp_gt_u32_e32 vcc, s14, v51
	v_lshlrev_b32_e32 v52, 3, v51
	s_and_b64 exec, s[38:39], vcc
	ds_write_b64 v52, v[10:11] offset:14336
	s_mov_b64 exec, s[38:39]
	v_subrev_u32_e32 v51, 0x1000, v39
	v_cmp_gt_u32_e32 vcc, s14, v51
	v_lshlrev_b32_e32 v52, 3, v51
	s_and_b64 exec, s[38:39], vcc
	ds_write_b64 v52, v[12:13] offset:14336
	s_mov_b64 exec, s[38:39]
	v_subrev_u32_e32 v51, 0x1000, v40
	v_cmp_gt_u32_e32 vcc, s14, v51
	v_lshlrev_b32_e32 v52, 3, v51
	s_and_b64 exec, s[38:39], vcc
	ds_write_b64 v52, v[14:15] offset:14336
	s_mov_b64 exec, s[38:39]
	v_subrev_u32_e32 v51, 0x1000, v41
	v_cmp_gt_u32_e32 vcc, s14, v51
	v_lshlrev_b32_e32 v52, 3, v51
	s_and_b64 exec, s[38:39], vcc
	ds_write_b64 v52, v[16:17] offset:14336
	s_mov_b64 exec, s[38:39]
	v_subrev_u32_e32 v51, 0x1000, v42
	v_cmp_gt_u32_e32 vcc, s14, v51
	v_lshlrev_b32_e32 v52, 3, v51
	s_and_b64 exec, s[38:39], vcc
	ds_write_b64 v52, v[18:19] offset:14336
	s_mov_b64 exec, s[38:39]
	v_subrev_u32_e32 v51, 0x1000, v43
	v_cmp_gt_u32_e32 vcc, s14, v51
	v_lshlrev_b32_e32 v52, 3, v51
	s_and_b64 exec, s[38:39], vcc
	ds_write_b64 v52, v[20:21] offset:14336
	s_mov_b64 exec, s[38:39]
	v_subrev_u32_e32 v51, 0x1000, v44
	v_cmp_gt_u32_e32 vcc, s14, v51
	v_lshlrev_b32_e32 v52, 3, v51
	s_and_b64 exec, s[38:39], vcc
	ds_write_b64 v52, v[22:23] offset:14336
	s_mov_b64 exec, s[38:39]
	v_subrev_u32_e32 v51, 0x1000, v45
	v_cmp_gt_u32_e32 vcc, s14, v51
	v_lshlrev_b32_e32 v52, 3, v51
	s_and_b64 exec, s[38:39], vcc
	ds_write_b64 v52, v[24:25] offset:14336
	s_mov_b64 exec, s[38:39]
	v_subrev_u32_e32 v51, 0x1000, v46
	v_cmp_gt_u32_e32 vcc, s14, v51
	v_lshlrev_b32_e32 v52, 3, v51
	s_and_b64 exec, s[38:39], vcc
	ds_write_b64 v52, v[26:27] offset:14336
	s_mov_b64 exec, s[38:39]
	v_subrev_u32_e32 v51, 0x1000, v47
	v_cmp_gt_u32_e32 vcc, s14, v51
	v_lshlrev_b32_e32 v52, 3, v51
	s_and_b64 exec, s[38:39], vcc
	ds_write_b64 v52, v[28:29] offset:14336
	s_mov_b64 exec, s[38:39]
	v_subrev_u32_e32 v51, 0x1000, v48
	v_cmp_gt_u32_e32 vcc, s14, v51
	v_lshlrev_b32_e32 v52, 3, v51
	s_and_b64 exec, s[38:39], vcc
	ds_write_b64 v52, v[30:31] offset:14336
	s_mov_b64 exec, s[38:39]
	v_subrev_u32_e32 v51, 0x1000, v49
	v_cmp_gt_u32_e32 vcc, s14, v51
	v_lshlrev_b32_e32 v52, 3, v51
	s_and_b64 exec, s[38:39], vcc
	ds_write_b64 v52, v[32:33] offset:14336
	s_mov_b64 exec, s[38:39]
	s_waitcnt lgkmcnt(0)
	s_barrier
	v_mov_b32_e32 v61, v0
	v_lshlrev_b32_e32 v62, 3, v61
	ds_read_b64 v[50:51], v62 offset:14336
	s_waitcnt lgkmcnt(0)
	v_subrev_co_u32_e32 v53, vcc, 0x61a80, v51
	v_lshrrev_b32_e32 v53, 6, v53
	v_lshrrev_b32_e32 v54, 9, v51
	v_add_u32_e32 v53, 0x30e, v53
	v_cndmask_b32_e32 v53, v53, v54, vcc
	v_min_u32_e32 v53, 0x447, v53
	v_lshlrev_b32_e32 v53, 2, v53
	ds_read_b32 v53, v53
	v_cmp_le_i32_e32 vcc, 0, v51
	s_waitcnt lgkmcnt(0)
	v_add_u32_e32 v53, v53, v61
	v_add_u32_e32 v53, 0x1000, v53
	v_lshlrev_b32_e32 v53, 3, v53
	s_and_b64 exec, s[38:39], vcc
	global_store_dwordx2 v53, v[50:51], s[34:35]
	s_mov_b64 exec, s[38:39]
	v_add_u32_e32 v61, 0x400, v0
	v_lshlrev_b32_e32 v62, 3, v61
	ds_read_b64 v[50:51], v62 offset:14336
	s_waitcnt lgkmcnt(0)
	v_subrev_co_u32_e32 v53, vcc, 0x61a80, v51
	v_lshrrev_b32_e32 v53, 6, v53
	v_lshrrev_b32_e32 v54, 9, v51
	v_add_u32_e32 v53, 0x30e, v53
	v_cndmask_b32_e32 v53, v53, v54, vcc
	v_min_u32_e32 v53, 0x447, v53
	v_lshlrev_b32_e32 v53, 2, v53
	ds_read_b32 v53, v53
	v_cmp_le_i32_e32 vcc, 0, v51
	s_waitcnt lgkmcnt(0)
	v_add_u32_e32 v53, v53, v61
	v_add_u32_e32 v53, 0x1000, v53
	v_lshlrev_b32_e32 v53, 3, v53
	s_and_b64 exec, s[38:39], vcc
	global_store_dwordx2 v53, v[50:51], s[34:35]
	s_mov_b64 exec, s[38:39]
	v_add_u32_e32 v61, 0x800, v0
	v_lshlrev_b32_e32 v62, 3, v61
	ds_read_b64 v[50:51], v62 offset:14336
	s_waitcnt lgkmcnt(0)
	v_subrev_co_u32_e32 v53, vcc, 0x61a80, v51
	v_lshrrev_b32_e32 v53, 6, v53
	v_lshrrev_b32_e32 v54, 9, v51
	v_add_u32_e32 v53, 0x30e, v53
	v_cndmask_b32_e32 v53, v53, v54, vcc
	v_min_u32_e32 v53, 0x447, v53
	v_lshlrev_b32_e32 v53, 2, v53
	ds_read_b32 v53, v53
	v_cmp_le_i32_e32 vcc, 0, v51
	s_waitcnt lgkmcnt(0)
	v_add_u32_e32 v53, v53, v61
	v_add_u32_e32 v53, 0x1000, v53
	v_lshlrev_b32_e32 v53, 3, v53
	s_and_b64 exec, s[38:39], vcc
	global_store_dwordx2 v53, v[50:51], s[34:35]
	s_mov_b64 exec, s[38:39]
	v_add_u32_e32 v61, 0xc00, v0
	v_lshlrev_b32_e32 v62, 3, v61
	ds_read_b64 v[50:51], v62 offset:14336
	s_waitcnt lgkmcnt(0)
	v_subrev_co_u32_e32 v53, vcc, 0x61a80, v51
	v_lshrrev_b32_e32 v53, 6, v53
	v_lshrrev_b32_e32 v54, 9, v51
	v_add_u32_e32 v53, 0x30e, v53
	v_cndmask_b32_e32 v53, v53, v54, vcc
	v_min_u32_e32 v53, 0x447, v53
	v_lshlrev_b32_e32 v53, 2, v53
	ds_read_b32 v53, v53
	v_cmp_le_i32_e32 vcc, 0, v51
	s_waitcnt lgkmcnt(0)
	v_add_u32_e32 v53, v53, v61
	v_add_u32_e32 v53, 0x1000, v53
	v_lshlrev_b32_e32 v53, 3, v53
	s_and_b64 exec, s[38:39], vcc
	global_store_dwordx2 v53, v[50:51], s[34:35]
	s_mov_b64 exec, s[38:39]
	s_barrier
	v_subrev_u32_e32 v51, 0x2000, v34
	v_cmp_gt_u32_e32 vcc, s14, v51
	v_lshlrev_b32_e32 v52, 3, v51
	s_and_b64 exec, s[38:39], vcc
	ds_write_b64 v52, v[2:3] offset:14336
	s_mov_b64 exec, s[38:39]
	v_subrev_u32_e32 v51, 0x2000, v35
	v_cmp_gt_u32_e32 vcc, s14, v51
	v_lshlrev_b32_e32 v52, 3, v51
	s_and_b64 exec, s[38:39], vcc
	ds_write_b64 v52, v[4:5] offset:14336
	s_mov_b64 exec, s[38:39]
	v_subrev_u32_e32 v51, 0x2000, v36
	v_cmp_gt_u32_e32 vcc, s14, v51
	v_lshlrev_b32_e32 v52, 3, v51
	s_and_b64 exec, s[38:39], vcc
	ds_write_b64 v52, v[6:7] offset:14336
	s_mov_b64 exec, s[38:39]
	v_subrev_u32_e32 v51, 0x2000, v37
	v_cmp_gt_u32_e32 vcc, s14, v51
	v_lshlrev_b32_e32 v52, 3, v51
	s_and_b64 exec, s[38:39], vcc
	ds_write_b64 v52, v[8:9] offset:14336
	s_mov_b64 exec, s[38:39]
	v_subrev_u32_e32 v51, 0x2000, v38
	v_cmp_gt_u32_e32 vcc, s14, v51
	v_lshlrev_b32_e32 v52, 3, v51
	s_and_b64 exec, s[38:39], vcc
	ds_write_b64 v52, v[10:11] offset:14336
	s_mov_b64 exec, s[38:39]
	v_subrev_u32_e32 v51, 0x2000, v39
	v_cmp_gt_u32_e32 vcc, s14, v51
	v_lshlrev_b32_e32 v52, 3, v51
	s_and_b64 exec, s[38:39], vcc
	ds_write_b64 v52, v[12:13] offset:14336
	s_mov_b64 exec, s[38:39]
	v_subrev_u32_e32 v51, 0x2000, v40
	v_cmp_gt_u32_e32 vcc, s14, v51
	v_lshlrev_b32_e32 v52, 3, v51
	s_and_b64 exec, s[38:39], vcc
	ds_write_b64 v52, v[14:15] offset:14336
	s_mov_b64 exec, s[38:39]
	v_subrev_u32_e32 v51, 0x2000, v41
	v_cmp_gt_u32_e32 vcc, s14, v51
	v_lshlrev_b32_e32 v52, 3, v51
	s_and_b64 exec, s[38:39], vcc
	ds_write_b64 v52, v[16:17] offset:14336
	s_mov_b64 exec, s[38:39]
	v_subrev_u32_e32 v51, 0x2000, v42
	v_cmp_gt_u32_e32 vcc, s14, v51
	v_lshlrev_b32_e32 v52, 3, v51
	s_and_b64 exec, s[38:39], vcc
	ds_write_b64 v52, v[18:19] offset:14336
	s_mov_b64 exec, s[38:39]
	v_subrev_u32_e32 v51, 0x2000, v43
	v_cmp_gt_u32_e32 vcc, s14, v51
	v_lshlrev_b32_e32 v52, 3, v51
	s_and_b64 exec, s[38:39], vcc
	ds_write_b64 v52, v[20:21] offset:14336
	s_mov_b64 exec, s[38:39]
	v_subrev_u32_e32 v51, 0x2000, v44
	v_cmp_gt_u32_e32 vcc, s14, v51
	v_lshlrev_b32_e32 v52, 3, v51
	s_and_b64 exec, s[38:39], vcc
	ds_write_b64 v52, v[22:23] offset:14336
	s_mov_b64 exec, s[38:39]
	v_subrev_u32_e32 v51, 0x2000, v45
	v_cmp_gt_u32_e32 vcc, s14, v51
	v_lshlrev_b32_e32 v52, 3, v51
	s_and_b64 exec, s[38:39], vcc
	ds_write_b64 v52, v[24:25] offset:14336
	s_mov_b64 exec, s[38:39]
	v_subrev_u32_e32 v51, 0x2000, v46
	v_cmp_gt_u32_e32 vcc, s14, v51
	v_lshlrev_b32_e32 v52, 3, v51
	s_and_b64 exec, s[38:39], vcc
	ds_write_b64 v52, v[26:27] offset:14336
	s_mov_b64 exec, s[38:39]
	v_subrev_u32_e32 v51, 0x2000, v47
	v_cmp_gt_u32_e32 vcc, s14, v51
	v_lshlrev_b32_e32 v52, 3, v51
	s_and_b64 exec, s[38:39], vcc
	ds_write_b64 v52, v[28:29] offset:14336
	s_mov_b64 exec, s[38:39]
	v_subrev_u32_e32 v51, 0x2000, v48
	v_cmp_gt_u32_e32 vcc, s14, v51
	v_lshlrev_b32_e32 v52, 3, v51
	s_and_b64 exec, s[38:39], vcc
	ds_write_b64 v52, v[30:31] offset:14336
	s_mov_b64 exec, s[38:39]
	v_subrev_u32_e32 v51, 0x2000, v49
	v_cmp_gt_u32_e32 vcc, s14, v51
	v_lshlrev_b32_e32 v52, 3, v51
	s_and_b64 exec, s[38:39], vcc
	ds_write_b64 v52, v[32:33] offset:14336
	s_mov_b64 exec, s[38:39]
	s_waitcnt lgkmcnt(0)
	s_barrier
	v_mov_b32_e32 v61, v0
	v_lshlrev_b32_e32 v62, 3, v61
	ds_read_b64 v[50:51], v62 offset:14336
	s_waitcnt lgkmcnt(0)
	v_subrev_co_u32_e32 v53, vcc, 0x61a80, v51
	v_lshrrev_b32_e32 v53, 6, v53
	v_lshrrev_b32_e32 v54, 9, v51
	v_add_u32_e32 v53, 0x30e, v53
	v_cndmask_b32_e32 v53, v53, v54, vcc
	v_min_u32_e32 v53, 0x447, v53
	v_lshlrev_b32_e32 v53, 2, v53
	ds_read_b32 v53, v53
	v_cmp_le_i32_e32 vcc, 0, v51
	s_waitcnt lgkmcnt(0)
	v_add_u32_e32 v53, v53, v61
	v_add_u32_e32 v53, 0x2000, v53
	v_lshlrev_b32_e32 v53, 3, v53
	s_and_b64 exec, s[38:39], vcc
	global_store_dwordx2 v53, v[50:51], s[34:35]
	s_mov_b64 exec, s[38:39]
	v_add_u32_e32 v61, 0x400, v0
	v_lshlrev_b32_e32 v62, 3, v61
	ds_read_b64 v[50:51], v62 offset:14336
	s_waitcnt lgkmcnt(0)
	v_subrev_co_u32_e32 v53, vcc, 0x61a80, v51
	v_lshrrev_b32_e32 v53, 6, v53
	v_lshrrev_b32_e32 v54, 9, v51
	v_add_u32_e32 v53, 0x30e, v53
	v_cndmask_b32_e32 v53, v53, v54, vcc
	v_min_u32_e32 v53, 0x447, v53
	v_lshlrev_b32_e32 v53, 2, v53
	ds_read_b32 v53, v53
	v_cmp_le_i32_e32 vcc, 0, v51
	s_waitcnt lgkmcnt(0)
	v_add_u32_e32 v53, v53, v61
	v_add_u32_e32 v53, 0x2000, v53
	v_lshlrev_b32_e32 v53, 3, v53
	s_and_b64 exec, s[38:39], vcc
	global_store_dwordx2 v53, v[50:51], s[34:35]
	s_mov_b64 exec, s[38:39]
	v_add_u32_e32 v61, 0x800, v0
	v_lshlrev_b32_e32 v62, 3, v61
	ds_read_b64 v[50:51], v62 offset:14336
	s_waitcnt lgkmcnt(0)
	v_subrev_co_u32_e32 v53, vcc, 0x61a80, v51
	v_lshrrev_b32_e32 v53, 6, v53
	v_lshrrev_b32_e32 v54, 9, v51
	v_add_u32_e32 v53, 0x30e, v53
	v_cndmask_b32_e32 v53, v53, v54, vcc
	v_min_u32_e32 v53, 0x447, v53
	v_lshlrev_b32_e32 v53, 2, v53
	ds_read_b32 v53, v53
	v_cmp_le_i32_e32 vcc, 0, v51
	s_waitcnt lgkmcnt(0)
	v_add_u32_e32 v53, v53, v61
	v_add_u32_e32 v53, 0x2000, v53
	v_lshlrev_b32_e32 v53, 3, v53
	s_and_b64 exec, s[38:39], vcc
	global_store_dwordx2 v53, v[50:51], s[34:35]
	s_mov_b64 exec, s[38:39]
	v_add_u32_e32 v61, 0xc00, v0
	v_lshlrev_b32_e32 v62, 3, v61
	ds_read_b64 v[50:51], v62 offset:14336
	s_waitcnt lgkmcnt(0)
	v_subrev_co_u32_e32 v53, vcc, 0x61a80, v51
	v_lshrrev_b32_e32 v53, 6, v53
	v_lshrrev_b32_e32 v54, 9, v51
	v_add_u32_e32 v53, 0x30e, v53
	v_cndmask_b32_e32 v53, v53, v54, vcc
	v_min_u32_e32 v53, 0x447, v53
	v_lshlrev_b32_e32 v53, 2, v53
	ds_read_b32 v53, v53
	v_cmp_le_i32_e32 vcc, 0, v51
	s_waitcnt lgkmcnt(0)
	v_add_u32_e32 v53, v53, v61
	v_add_u32_e32 v53, 0x2000, v53
	v_lshlrev_b32_e32 v53, 3, v53
	s_and_b64 exec, s[38:39], vcc
	global_store_dwordx2 v53, v[50:51], s[34:35]
	s_mov_b64 exec, s[38:39]
	s_barrier
	v_subrev_u32_e32 v51, 0x3000, v34
	v_cmp_gt_u32_e32 vcc, s14, v51
	v_lshlrev_b32_e32 v52, 3, v51
	s_and_b64 exec, s[38:39], vcc
	ds_write_b64 v52, v[2:3] offset:14336
	s_mov_b64 exec, s[38:39]
	v_subrev_u32_e32 v51, 0x3000, v35
	v_cmp_gt_u32_e32 vcc, s14, v51
	v_lshlrev_b32_e32 v52, 3, v51
	s_and_b64 exec, s[38:39], vcc
	ds_write_b64 v52, v[4:5] offset:14336
	s_mov_b64 exec, s[38:39]
	v_subrev_u32_e32 v51, 0x3000, v36
	v_cmp_gt_u32_e32 vcc, s14, v51
	v_lshlrev_b32_e32 v52, 3, v51
	s_and_b64 exec, s[38:39], vcc
	ds_write_b64 v52, v[6:7] offset:14336
	s_mov_b64 exec, s[38:39]
	v_subrev_u32_e32 v51, 0x3000, v37
	v_cmp_gt_u32_e32 vcc, s14, v51
	v_lshlrev_b32_e32 v52, 3, v51
	s_and_b64 exec, s[38:39], vcc
	ds_write_b64 v52, v[8:9] offset:14336
	s_mov_b64 exec, s[38:39]
	v_subrev_u32_e32 v51, 0x3000, v38
	v_cmp_gt_u32_e32 vcc, s14, v51
	v_lshlrev_b32_e32 v52, 3, v51
	s_and_b64 exec, s[38:39], vcc
	ds_write_b64 v52, v[10:11] offset:14336
	s_mov_b64 exec, s[38:39]
	v_subrev_u32_e32 v51, 0x3000, v39
	v_cmp_gt_u32_e32 vcc, s14, v51
	v_lshlrev_b32_e32 v52, 3, v51
	s_and_b64 exec, s[38:39], vcc
	ds_write_b64 v52, v[12:13] offset:14336
	s_mov_b64 exec, s[38:39]
	v_subrev_u32_e32 v51, 0x3000, v40
	v_cmp_gt_u32_e32 vcc, s14, v51
	v_lshlrev_b32_e32 v52, 3, v51
	s_and_b64 exec, s[38:39], vcc
	ds_write_b64 v52, v[14:15] offset:14336
	s_mov_b64 exec, s[38:39]
	v_subrev_u32_e32 v51, 0x3000, v41
	v_cmp_gt_u32_e32 vcc, s14, v51
	v_lshlrev_b32_e32 v52, 3, v51
	s_and_b64 exec, s[38:39], vcc
	ds_write_b64 v52, v[16:17] offset:14336
	s_mov_b64 exec, s[38:39]
	v_subrev_u32_e32 v51, 0x3000, v42
	v_cmp_gt_u32_e32 vcc, s14, v51
	v_lshlrev_b32_e32 v52, 3, v51
	s_and_b64 exec, s[38:39], vcc
	ds_write_b64 v52, v[18:19] offset:14336
	s_mov_b64 exec, s[38:39]
	v_subrev_u32_e32 v51, 0x3000, v43
	v_cmp_gt_u32_e32 vcc, s14, v51
	v_lshlrev_b32_e32 v52, 3, v51
	s_and_b64 exec, s[38:39], vcc
	ds_write_b64 v52, v[20:21] offset:14336
	s_mov_b64 exec, s[38:39]
	v_subrev_u32_e32 v51, 0x3000, v44
	v_cmp_gt_u32_e32 vcc, s14, v51
	v_lshlrev_b32_e32 v52, 3, v51
	s_and_b64 exec, s[38:39], vcc
	ds_write_b64 v52, v[22:23] offset:14336
	s_mov_b64 exec, s[38:39]
	v_subrev_u32_e32 v51, 0x3000, v45
	v_cmp_gt_u32_e32 vcc, s14, v51
	v_lshlrev_b32_e32 v52, 3, v51
	s_and_b64 exec, s[38:39], vcc
	ds_write_b64 v52, v[24:25] offset:14336
	s_mov_b64 exec, s[38:39]
	v_subrev_u32_e32 v51, 0x3000, v46
	v_cmp_gt_u32_e32 vcc, s14, v51
	v_lshlrev_b32_e32 v52, 3, v51
	s_and_b64 exec, s[38:39], vcc
	ds_write_b64 v52, v[26:27] offset:14336
	s_mov_b64 exec, s[38:39]
	v_subrev_u32_e32 v51, 0x3000, v47
	v_cmp_gt_u32_e32 vcc, s14, v51
	v_lshlrev_b32_e32 v52, 3, v51
	s_and_b64 exec, s[38:39], vcc
	ds_write_b64 v52, v[28:29] offset:14336
	s_mov_b64 exec, s[38:39]
	v_subrev_u32_e32 v51, 0x3000, v48
	v_cmp_gt_u32_e32 vcc, s14, v51
	v_lshlrev_b32_e32 v52, 3, v51
	s_and_b64 exec, s[38:39], vcc
	ds_write_b64 v52, v[30:31] offset:14336
	s_mov_b64 exec, s[38:39]
	v_subrev_u32_e32 v51, 0x3000, v49
	v_cmp_gt_u32_e32 vcc, s14, v51
	v_lshlrev_b32_e32 v52, 3, v51
	s_and_b64 exec, s[38:39], vcc
	ds_write_b64 v52, v[32:33] offset:14336
	s_mov_b64 exec, s[38:39]
	s_waitcnt lgkmcnt(0)
	s_barrier
	v_mov_b32_e32 v61, v0
	v_lshlrev_b32_e32 v62, 3, v61
	ds_read_b64 v[50:51], v62 offset:14336
	s_waitcnt lgkmcnt(0)
	v_subrev_co_u32_e32 v53, vcc, 0x61a80, v51
	v_lshrrev_b32_e32 v53, 6, v53
	v_lshrrev_b32_e32 v54, 9, v51
	v_add_u32_e32 v53, 0x30e, v53
	v_cndmask_b32_e32 v53, v53, v54, vcc
	v_min_u32_e32 v53, 0x447, v53
	v_lshlrev_b32_e32 v53, 2, v53
	ds_read_b32 v53, v53
	v_cmp_le_i32_e32 vcc, 0, v51
	s_waitcnt lgkmcnt(0)
	v_add_u32_e32 v53, v53, v61
	v_add_u32_e32 v53, 0x3000, v53
	v_lshlrev_b32_e32 v53, 3, v53
	s_and_b64 exec, s[38:39], vcc
	global_store_dwordx2 v53, v[50:51], s[34:35]
	s_mov_b64 exec, s[38:39]
	v_add_u32_e32 v61, 0x400, v0
	v_lshlrev_b32_e32 v62, 3, v61
	ds_read_b64 v[50:51], v62 offset:14336
	s_waitcnt lgkmcnt(0)
	v_subrev_co_u32_e32 v53, vcc, 0x61a80, v51
	v_lshrrev_b32_e32 v53, 6, v53
	v_lshrrev_b32_e32 v54, 9, v51
	v_add_u32_e32 v53, 0x30e, v53
	v_cndmask_b32_e32 v53, v53, v54, vcc
	v_min_u32_e32 v53, 0x447, v53
	v_lshlrev_b32_e32 v53, 2, v53
	ds_read_b32 v53, v53
	v_cmp_le_i32_e32 vcc, 0, v51
	s_waitcnt lgkmcnt(0)
	v_add_u32_e32 v53, v53, v61
	v_add_u32_e32 v53, 0x3000, v53
	v_lshlrev_b32_e32 v53, 3, v53
	s_and_b64 exec, s[38:39], vcc
	global_store_dwordx2 v53, v[50:51], s[34:35]
	s_mov_b64 exec, s[38:39]
	v_add_u32_e32 v61, 0x800, v0
	v_lshlrev_b32_e32 v62, 3, v61
	ds_read_b64 v[50:51], v62 offset:14336
	s_waitcnt lgkmcnt(0)
	v_subrev_co_u32_e32 v53, vcc, 0x61a80, v51
	v_lshrrev_b32_e32 v53, 6, v53
	v_lshrrev_b32_e32 v54, 9, v51
	v_add_u32_e32 v53, 0x30e, v53
	v_cndmask_b32_e32 v53, v53, v54, vcc
	v_min_u32_e32 v53, 0x447, v53
	v_lshlrev_b32_e32 v53, 2, v53
	ds_read_b32 v53, v53
	v_cmp_le_i32_e32 vcc, 0, v51
	s_waitcnt lgkmcnt(0)
	v_add_u32_e32 v53, v53, v61
	v_add_u32_e32 v53, 0x3000, v53
	v_lshlrev_b32_e32 v53, 3, v53
	s_and_b64 exec, s[38:39], vcc
	global_store_dwordx2 v53, v[50:51], s[34:35]
	s_mov_b64 exec, s[38:39]
	v_add_u32_e32 v61, 0xc00, v0
	v_lshlrev_b32_e32 v62, 3, v61
	ds_read_b64 v[50:51], v62 offset:14336
	s_waitcnt lgkmcnt(0)
	v_subrev_co_u32_e32 v53, vcc, 0x61a80, v51
	v_lshrrev_b32_e32 v53, 6, v53
	v_lshrrev_b32_e32 v54, 9, v51
	v_add_u32_e32 v53, 0x30e, v53
	v_cndmask_b32_e32 v53, v53, v54, vcc
	v_min_u32_e32 v53, 0x447, v53
	v_lshlrev_b32_e32 v53, 2, v53
	ds_read_b32 v53, v53
	v_cmp_le_i32_e32 vcc, 0, v51
	s_waitcnt lgkmcnt(0)
	v_add_u32_e32 v53, v53, v61
	v_add_u32_e32 v53, 0x3000, v53
	v_lshlrev_b32_e32 v53, 3, v53
	s_and_b64 exec, s[38:39], vcc
	global_store_dwordx2 v53, v[50:51], s[34:35]
	s_mov_b64 exec, s[38:39]
	s_endpgm

.LBB2_355:
	s_cbranch_execz .LBB2_132
	s_branch .LBB2_354
	.section	.rodata,"a",@progbits
	.p2align	6, 0x0
	.amdhsa_kernel _Z6k_prepPKiS0_S0_S0_PiP15HIP_vector_typeIiLj2EEPKfS6_S0_S0_S0_S6_S6_S6_PDF16_S7_6WSpecs
		.amdhsa_group_segment_fixed_size 47104
		.amdhsa_private_segment_fixed_size 0
		.amdhsa_kernarg_size 616
		.amdhsa_user_sgpr_count 2
		.amdhsa_user_sgpr_dispatch_ptr 0
		.amdhsa_user_sgpr_queue_ptr 0
		.amdhsa_user_sgpr_kernarg_segment_ptr 1
		.amdhsa_user_sgpr_dispatch_id 0
		.amdhsa_user_sgpr_kernarg_preload_length 0
		.amdhsa_user_sgpr_kernarg_preload_offset 0
		.amdhsa_user_sgpr_private_segment_size 0
		.amdhsa_uses_dynamic_stack 0
		.amdhsa_enable_private_segment 0
		.amdhsa_system_sgpr_workgroup_id_x 1
		.amdhsa_system_sgpr_workgroup_id_y 0
		.amdhsa_system_sgpr_workgroup_id_z 0
		.amdhsa_system_sgpr_workgroup_info 0
		.amdhsa_system_vgpr_workitem_id 0
		.amdhsa_next_free_vgpr 88
		.amdhsa_next_free_sgpr 40
		.amdhsa_accum_offset 88
		.amdhsa_reserve_vcc 1
		.amdhsa_float_round_mode_32 0
		.amdhsa_float_round_mode_16_64 0
		.amdhsa_float_denorm_mode_32 3
		.amdhsa_float_denorm_mode_16_64 3
		.amdhsa_dx10_clamp 1
		.amdhsa_ieee_mode 1
		.amdhsa_fp16_overflow 0
		.amdhsa_tg_split 0
		.amdhsa_exception_fp_ieee_invalid_op 0
		.amdhsa_exception_fp_denorm_src 0
		.amdhsa_exception_fp_ieee_div_zero 0
		.amdhsa_exception_fp_ieee_overflow 0
		.amdhsa_exception_fp_ieee_underflow 0
		.amdhsa_exception_fp_ieee_inexact 0
		.amdhsa_exception_int_div_zero 0
	.end_amdhsa_kernel

amdhsa.kernels:
  - .agpr_count:     0
    .args:
      - .actual_access:  read_only
        .address_space:  global
        .offset:         0
        .size:           8
        .value_kind:     global_buffer
      - .actual_access:  read_only
        .address_space:  global
        .offset:         8
        .size:           8
        .value_kind:     global_buffer
      - .actual_access:  write_only
        .address_space:  global
        .offset:         16
        .size:           8
        .value_kind:     global_buffer
      - .address_space:  global
        .offset:         24
        .size:           8
        .value_kind:     global_buffer
    .group_segment_fixed_size: 20736
    .kernarg_segment_align: 8
    .kernarg_segment_size: 32
    .language:       OpenCL C
    .language_version:
      - 2
      - 0
    .max_flat_workgroup_size: 256
    .name:           _Z6k_bcsrPK15HIP_vector_typeIiLj2EEPKiPiS5_
    .private_segment_fixed_size: 0
    .sgpr_count:     40
    .sgpr_spill_count: 0
    .symbol:         _Z6k_bcsrPK15HIP_vector_typeIiLj2EEPKiPiS5_.kd
    .uniform_work_group_size: 1
    .uses_dynamic_stack: false
    .vgpr_count:     64
    .vgpr_spill_count: 0
    .wavefront_size: 64
  - .agpr_count:     0
    .args:
      - .actual_access:  read_only
        .address_space:  global
        .offset:         0
        .size:           8
        .value_kind:     global_buffer
      - .actual_access:  read_only
        .address_space:  global
        .offset:         8
        .size:           8
        .value_kind:     global_buffer
      - .actual_access:  read_only
        .address_space:  global
        .offset:         16
        .size:           8
        .value_kind:     global_buffer
      - .actual_access:  write_only
        .address_space:  global
        .offset:         24
        .size:           8
        .value_kind:     global_buffer
      - .actual_access:  write_only
        .address_space:  global
        .offset:         32
        .size:           8
        .value_kind:     global_buffer
      - .actual_access:  read_only
        .address_space:  global
        .offset:         40
        .size:           8
        .value_kind:     global_buffer
      - .actual_access:  read_only
        .address_space:  global
        .offset:         48
        .size:           8
        .value_kind:     global_buffer
      - .actual_access:  read_only
        .address_space:  global
        .offset:         56
        .size:           8
        .value_kind:     global_buffer
      - .actual_access:  read_only
        .address_space:  global
        .offset:         64
        .size:           8
        .value_kind:     global_buffer
      - .actual_access:  read_only
        .address_space:  global
        .offset:         72
        .size:           8
        .value_kind:     global_buffer
      - .actual_access:  read_only
        .address_space:  global
        .offset:         80
        .size:           8
        .value_kind:     global_buffer
      - .actual_access:  read_only
        .address_space:  global
        .offset:         88
        .size:           8
        .value_kind:     global_buffer
      - .actual_access:  read_only
        .address_space:  global
        .offset:         96
        .size:           8
        .value_kind:     global_buffer
      - .address_space:  global
        .offset:         104
        .size:           8
        .value_kind:     global_buffer
      - .address_space:  global
        .offset:         112
        .size:           8
        .value_kind:     global_buffer
    .group_segment_fixed_size: 4384
    .kernarg_segment_align: 8
    .kernarg_segment_size: 120
    .language:       OpenCL C
    .language_version:
      - 2
      - 0
    .max_flat_workgroup_size: 1024
    .name:           _Z8k_bcountPKiS0_S0_PiPjPKfS4_S0_S0_S0_S4_S4_S4_PDF16_S5_
    .private_segment_fixed_size: 0
    .sgpr_count:     26
    .sgpr_spill_count: 0
    .symbol:         _Z8k_bcountPKiS0_S0_PiPjPKfS4_S0_S0_S0_S4_S4_S4_PDF16_S5_.kd
    .uniform_work_group_size: 1
    .uses_dynamic_stack: false
    .vgpr_count:     41
    .vgpr_spill_count: 0
    .wavefront_size: 64
  - .agpr_count:     0
    .args:
      - .actual_access:  read_only
        .address_space:  global
        .offset:         0
        .size:           8
        .value_kind:     global_buffer
      - .actual_access:  read_only
        .address_space:  global
        .offset:         8
        .size:           8
        .value_kind:     global_buffer
      - .actual_access:  read_only
        .address_space:  global
        .offset:         16
        .size:           8
        .value_kind:     global_buffer
      - .actual_access:  read_only
        .address_space:  global
        .offset:         24
        .size:           8
        .value_kind:     global_buffer
      - .actual_access:  write_only
        .address_space:  global
        .offset:         32
        .size:           8
        .value_kind:     global_buffer
      - .actual_access:  write_only
        .address_space:  global
        .offset:         40
        .size:           8
        .value_kind:     global_buffer
      - .actual_access:  read_only
        .address_space:  global
        .offset:         48
        .size:           8
        .value_kind:     global_buffer
      - .actual_access:  read_only
        .address_space:  global
        .offset:         56
        .size:           8
        .value_kind:     global_buffer
      - .actual_access:  read_only
        .address_space:  global
        .offset:         64
        .size:           8
        .value_kind:     global_buffer
      - .actual_access:  read_only
        .address_space:  global
        .offset:         72
        .size:           8
        .value_kind:     global_buffer
      - .actual_access:  read_only
        .address_space:  global
        .offset:         80
        .size:           8
        .value_kind:     global_buffer
      - .actual_access:  read_only
        .address_space:  global
        .offset:         88
        .size:           8
        .value_kind:     global_buffer
      - .actual_access:  read_only
        .address_space:  global
        .offset:         96
        .size:           8
        .value_kind:     global_buffer
      - .actual_access:  read_only
        .address_space:  global
        .offset:         104
        .size:           8
        .value_kind:     global_buffer
      - .address_space:  global
        .offset:         112
        .size:           8
        .value_kind:     global_buffer
      - .address_space:  global
        .offset:         120
        .size:           8
        .value_kind:     global_buffer
      - .offset:         128
        .size:           488
        .value_kind:     by_value
    .group_segment_fixed_size: 47104
    .kernarg_segment_align: 8
    .kernarg_segment_size: 616
    .language:       OpenCL C
    .language_version:
      - 2
      - 0
    .max_flat_workgroup_size: 1024
    .name:           _Z6k_prepPKiS0_S0_S0_PiP15HIP_vector_typeIiLj2EEPKfS6_S0_S0_S0_S6_S6_S6_PDF16_S7_6WSpecs
    .private_segment_fixed_size: 0
    .sgpr_count:     44
    .sgpr_spill_count: 0
    .symbol:         _Z6k_prepPKiS0_S0_S0_PiP15HIP_vector_typeIiLj2EEPKfS6_S0_S0_S0_S6_S6_S6_PDF16_S7_6WSpecs.kd
    .uniform_work_group_size: 1
    .uses_dynamic_stack: false
    .vgpr_count:     88
    .vgpr_spill_count: 0
    .wavefront_size: 64
  - .agpr_count:     0
    .args:
      - .offset:         0
        .size:           104
        .value_kind:     by_value
      - .offset:         104
        .size:           4
        .value_kind:     hidden_block_count_x
      - .offset:         108
        .size:           4
        .value_kind:     hidden_block_count_y
      - .offset:         112
        .size:           4
        .value_kind:     hidden_block_count_z
      - .offset:         116
        .size:           2
        .value_kind:     hidden_group_size_x
      - .offset:         118
        .size:           2
        .value_kind:     hidden_group_size_y
      - .offset:         120
        .size:           2
        .value_kind:     hidden_group_size_z
      - .offset:         122
        .size:           2
        .value_kind:     hidden_remainder_x
      - .offset:         124
        .size:           2
        .value_kind:     hidden_remainder_y
      - .offset:         126
        .size:           2
        .value_kind:     hidden_remainder_z
      - .offset:         144
        .size:           8
        .value_kind:     hidden_global_offset_x
      - .offset:         152
        .size:           8
        .value_kind:     hidden_global_offset_y
      - .offset:         160
        .size:           8
        .value_kind:     hidden_global_offset_z
      - .offset:         168
        .size:           2
        .value_kind:     hidden_grid_dims
    .group_segment_fixed_size: 155140
    .kernarg_segment_align: 8
    .kernarg_segment_size: 360
    .language:       OpenCL C
    .language_version:
      - 2
      - 0
    .max_flat_workgroup_size: 768
    .name:           _Z12k_layer_pool9LayerArgs
    .private_segment_fixed_size: 0
    .sgpr_count:     50
    .sgpr_spill_count: 0
    .symbol:         _Z12k_layer_pool9LayerArgs.kd
    .uniform_work_group_size: 1
    .uses_dynamic_stack: false
    .vgpr_count:     168
    .vgpr_spill_count: 0
    .wavefront_size: 64
  - .agpr_count:     0
    .args:
      - .actual_access:  read_only
        .address_space:  global
        .offset:         0
        .size:           8
        .value_kind:     global_buffer
      - .actual_access:  read_only
        .address_space:  global
        .offset:         8
        .size:           8
        .value_kind:     global_buffer
      - .actual_access:  read_only
        .address_space:  global
        .offset:         16
        .size:           8
        .value_kind:     global_buffer
      - .actual_access:  read_only
        .address_space:  global
        .offset:         24
        .size:           8
        .value_kind:     global_buffer
      - .actual_access:  read_only
        .address_space:  global
        .offset:         32
        .size:           8
        .value_kind:     global_buffer
      - .actual_access:  read_only
        .address_space:  global
        .offset:         40
        .size:           8
        .value_kind:     global_buffer
      - .actual_access:  read_only
        .address_space:  global
        .offset:         48
        .size:           8
        .value_kind:     global_buffer
      - .actual_access:  write_only
        .address_space:  global
        .offset:         56
        .size:           8
        .value_kind:     global_buffer
    .group_segment_fixed_size: 2560
    .kernarg_segment_align: 8
    .kernarg_segment_size: 64
    .language:       OpenCL C
    .language_version:
      - 2
      - 0
    .max_flat_workgroup_size: 512
    .name:           _Z5k_mlpPKjPKfS2_S2_S2_S2_S2_Pf
    .private_segment_fixed_size: 0
    .sgpr_count:     18
    .sgpr_spill_count: 0
    .symbol:         _Z5k_mlpPKjPKfS2_S2_S2_S2_S2_Pf.kd
    .uniform_work_group_size: 1
    .uses_dynamic_stack: false
    .vgpr_count:     120
    .vgpr_spill_count: 0
    .wavefront_size: 64
  - .agpr_count:     0
    .args:
      - .offset:         0
        .size:           104
        .value_kind:     by_value
      - .offset:         104
        .size:           104
        .value_kind:     by_value
      - .offset:         208
        .size:           4
        .value_kind:     by_value
      - .offset:         216
        .size:           4
        .value_kind:     hidden_block_count_x
      - .offset:         220
        .size:           4
        .value_kind:     hidden_block_count_y
      - .offset:         224
        .size:           4
        .value_kind:     hidden_block_count_z
      - .offset:         228
        .size:           2
        .value_kind:     hidden_group_size_x
      - .offset:         230
        .size:           2
        .value_kind:     hidden_group_size_y
      - .offset:         232
        .size:           2
        .value_kind:     hidden_group_size_z
      - .offset:         234
        .size:           2
        .value_kind:     hidden_remainder_x
      - .offset:         236
        .size:           2
        .value_kind:     hidden_remainder_y
      - .offset:         238
        .size:           2
        .value_kind:     hidden_remainder_z
      - .offset:         256
        .size:           8
        .value_kind:     hidden_global_offset_x
      - .offset:         264
        .size:           8
        .value_kind:     hidden_global_offset_y
      - .offset:         272
        .size:           8
        .value_kind:     hidden_global_offset_z
      - .offset:         280
        .size:           2
        .value_kind:     hidden_grid_dims
    .group_segment_fixed_size: 151044
    .kernarg_segment_align: 8
    .kernarg_segment_size: 472
    .language:       OpenCL C
    .language_version:
      - 2
      - 0
    .max_flat_workgroup_size: 768
    .name:           _Z10k_layer_fhILi96ELb1EEv9LayerArgsS0_i
    .private_segment_fixed_size: 0
    .sgpr_count:     52
    .sgpr_spill_count: 0
    .symbol:         _Z10k_layer_fhILi96ELb1EEv9LayerArgsS0_i.kd
    .uniform_work_group_size: 1
    .uses_dynamic_stack: false
    .vgpr_count:     168
    .vgpr_spill_count: 0
    .wavefront_size: 64
  - .agpr_count:     0
    .args:
      - .offset:         0
        .size:           104
        .value_kind:     by_value
      - .offset:         104
        .size:           104
        .value_kind:     by_value
      - .offset:         208
        .size:           4
        .value_kind:     by_value
      - .offset:         216
        .size:           4
        .value_kind:     hidden_block_count_x
      - .offset:         220
        .size:           4
        .value_kind:     hidden_block_count_y
      - .offset:         224
        .size:           4
        .value_kind:     hidden_block_count_z
      - .offset:         228
        .size:           2
        .value_kind:     hidden_group_size_x
      - .offset:         230
        .size:           2
        .value_kind:     hidden_group_size_y
      - .offset:         232
        .size:           2
        .value_kind:     hidden_group_size_z
      - .offset:         234
        .size:           2
        .value_kind:     hidden_remainder_x
      - .offset:         236
        .size:           2
        .value_kind:     hidden_remainder_y
      - .offset:         238
        .size:           2
        .value_kind:     hidden_remainder_z
      - .offset:         256
        .size:           8
        .value_kind:     hidden_global_offset_x
      - .offset:         264
        .size:           8
        .value_kind:     hidden_global_offset_y
      - .offset:         272
        .size:           8
        .value_kind:     hidden_global_offset_z
      - .offset:         280
        .size:           2
        .value_kind:     hidden_grid_dims
    .group_segment_fixed_size: 151044
    .kernarg_segment_align: 8
    .kernarg_segment_size: 472
    .language:       OpenCL C
    .language_version:
      - 2
      - 0
    .max_flat_workgroup_size: 768
    .name:           _Z10k_layer_fhILi128ELb1EEv9LayerArgsS0_i
    .private_segment_fixed_size: 0
    .sgpr_count:     45
    .sgpr_spill_count: 0
    .symbol:         _Z10k_layer_fhILi128ELb1EEv9LayerArgsS0_i.kd
    .uniform_work_group_size: 1
    .uses_dynamic_stack: false
    .vgpr_count:     168
    .vgpr_spill_count: 0
    .wavefront_size: 64
